# v41: v40 + LDS-DMA offset operands used directly (92 v_mov copies removed from GEMM K-loops)
# speedup vs baseline: 1.0112x; 1.0031x over previous
.LBB0_689:
	s_add_u32 s26, s21, s10
	s_addc_u32 s27, s22, s11
	s_add_u32 s12, s26, 0x15000100
	s_addc_u32 s13, s27, 0
	s_add_u32 s14, s23, s10
	s_addc_u32 s15, s24, s11
	s_add_i32 s28, 0, 0x10000
	s_cmpk_eq_i32 s10, 0x300
	s_cselect_b32 s13, s9, s13
	s_cselect_b32 s12, s8, s12
	v_add_u32_e32 v0, s28, v38
	s_cselect_b32 s15, s7, s15
	s_cselect_b32 s14, s6, s14
	s_add_i32 s29, 0, 0x14000
	ds_read_b128 v[138:141], v0
	ds_read_b128 v[142:145], v0 offset:1024
	ds_read_b128 v[146:149], v0 offset:2048
	ds_read_b128 v[150:153], v0 offset:3072
	v_add_u32_e32 v0, s29, v38
	ds_read_b128 v[154:157], v0
	ds_read_b128 v[158:161], v0 offset:1024
	ds_read_b128 v[162:165], v0 offset:2048
	ds_read_b128 v[166:169], v0 offset:3072
	v_mov_b32_e32 v0, v34
	ds_read_b128 v[170:173], v39
	ds_read_b128 v[174:177], v39 offset:1024
	ds_read_b128 v[178:181], v39 offset:2048
	ds_read_b128 v[182:185], v39 offset:3072
	ds_read_b128 v[186:189], v39 offset:4096
	ds_read_b128 v[190:193], v39 offset:5120
	ds_read_b128 v[194:197], v39 offset:6144
	ds_read_b128 v[198:201], v39 offset:7168
	s_add_i32 m0, s85, 0xc000
	v_lshl_add_u64 v[40:41], s[26:27], 0, v[0:1]
	v_lshl_add_u64 v[40:41], v[40:41], 0, s[64:65]
	v_mov_b32_e32 v0, v36
	global_load_lds_dwordx4 v[40:41], off
	s_add_i32 m0, s85, 0xe000
	v_lshl_add_u64 v[40:41], s[26:27], 0, v[0:1]
	v_lshl_add_u64 v[40:41], v[40:41], 0, s[64:65]
	global_load_lds_dwordx4 v[40:41], off
	s_waitcnt vmcnt(8)
	s_waitcnt lgkmcnt(0)
	s_barrier
	s_setprio 1
	s_waitcnt lgkmcnt(0)
	v_mfma_i32_16x16x64_i8 v[134:137], v[138:141], v[170:173], v[134:137]
	v_mfma_i32_16x16x64_i8 v[130:133], v[146:149], v[170:173], v[130:133]
	v_mfma_i32_16x16x64_i8 v[126:129], v[138:141], v[178:181], v[126:129]
	v_mfma_i32_16x16x64_i8 v[122:125], v[146:149], v[178:181], v[122:125]
	v_mfma_i32_16x16x64_i8 v[118:121], v[138:141], v[186:189], v[118:121]
	v_mfma_i32_16x16x64_i8 v[114:117], v[146:149], v[186:189], v[114:117]
	v_mfma_i32_16x16x64_i8 v[110:113], v[138:141], v[194:197], v[110:113]
	v_mfma_i32_16x16x64_i8 v[106:109], v[146:149], v[194:197], v[106:109]
	v_mfma_i32_16x16x64_i8 v[134:137], v[142:145], v[174:177], v[134:137]
	v_mfma_i32_16x16x64_i8 v[130:133], v[150:153], v[174:177], v[130:133]
	v_mfma_i32_16x16x64_i8 v[126:129], v[142:145], v[182:185], v[126:129]
	v_mfma_i32_16x16x64_i8 v[122:125], v[150:153], v[182:185], v[122:125]
	v_mfma_i32_16x16x64_i8 v[118:121], v[142:145], v[190:193], v[118:121]
	v_mfma_i32_16x16x64_i8 v[114:117], v[150:153], v[190:193], v[114:117]
	v_mfma_i32_16x16x64_i8 v[110:113], v[142:145], v[198:201], v[110:113]
	v_mfma_i32_16x16x64_i8 v[106:109], v[150:153], v[198:201], v[106:109]
	s_setprio 0
	s_setprio 1
	v_mfma_i32_16x16x64_i8 v[78:81], v[154:157], v[170:173], v[78:81]
	v_mfma_i32_16x16x64_i8 v[74:77], v[162:165], v[170:173], v[74:77]
	v_mfma_i32_16x16x64_i8 v[62:65], v[154:157], v[178:181], v[62:65]
	v_mfma_i32_16x16x64_i8 v[58:61], v[162:165], v[178:181], v[58:61]
	v_mfma_i32_16x16x64_i8 v[54:57], v[154:157], v[186:189], v[54:57]
	v_mfma_i32_16x16x64_i8 v[50:53], v[162:165], v[186:189], v[50:53]
	v_mfma_i32_16x16x64_i8 v[46:49], v[154:157], v[194:197], v[46:49]
	v_mfma_i32_16x16x64_i8 v[40:43], v[162:165], v[194:197], v[42:45]
	v_mfma_i32_16x16x64_i8 v[78:81], v[158:161], v[174:177], v[78:81]
	v_mfma_i32_16x16x64_i8 v[74:77], v[166:169], v[174:177], v[74:77]
	v_mfma_i32_16x16x64_i8 v[62:65], v[158:161], v[182:185], v[62:65]
	v_mfma_i32_16x16x64_i8 v[58:61], v[166:169], v[182:185], v[58:61]
	v_mfma_i32_16x16x64_i8 v[54:57], v[158:161], v[190:193], v[54:57]
	v_mfma_i32_16x16x64_i8 v[50:53], v[166:169], v[190:193], v[50:53]
	v_mfma_i32_16x16x64_i8 v[46:49], v[158:161], v[198:201], v[46:49]
	v_mfma_i32_16x16x64_i8 v[40:43], v[166:169], v[198:201], v[40:43]
	s_setprio 0
	s_barrier
	s_add_i32 s26, s28, s33
	ds_read_b128 v[170:173], v39 offset:16384
	ds_read_b128 v[174:177], v39 offset:17408
	ds_read_b128 v[178:181], v39 offset:18432
	ds_read_b128 v[182:185], v39 offset:19456
	ds_read_b128 v[186:189], v39 offset:20480
	ds_read_b128 v[190:193], v39 offset:21504
	ds_read_b128 v[194:197], v39 offset:22528
	ds_read_b128 v[198:201], v39 offset:23552
	s_mov_b32 m0, s26
	s_nop 0
	global_load_lds_dwordx4 v35, s[14:15]
	s_add_i32 m0, s26, 0x2000
	s_add_u32 s26, s14, 0x20000
	global_load_lds_dwordx4 v37, s[14:15]
	s_addc_u32 s27, s15, 0
	s_add_i32 s28, s29, s33
	s_mov_b32 m0, s28
	s_nop 0
	global_load_lds_dwordx4 v35, s[26:27]
	s_add_i32 m0, s28, 0x2000
	s_nop 0
	global_load_lds_dwordx4 v37, s[26:27]
	s_waitcnt vmcnt(6)
	s_waitcnt lgkmcnt(0)
	s_barrier
	s_setprio 1
	s_waitcnt lgkmcnt(0)
	v_mfma_i32_16x16x64_i8 v[102:105], v[138:141], v[170:173], v[102:105]
	v_mfma_i32_16x16x64_i8 v[98:101], v[146:149], v[170:173], v[98:101]
	v_mfma_i32_16x16x64_i8 v[94:97], v[138:141], v[178:181], v[94:97]
	v_mfma_i32_16x16x64_i8 v[90:93], v[146:149], v[178:181], v[90:93]
	v_mfma_i32_16x16x64_i8 v[86:89], v[138:141], v[186:189], v[86:89]
	v_mfma_i32_16x16x64_i8 v[82:85], v[146:149], v[186:189], v[82:85]
	v_mfma_i32_16x16x64_i8 v[70:73], v[138:141], v[194:197], v[70:73]
	v_mfma_i32_16x16x64_i8 v[66:69], v[146:149], v[194:197], v[66:69]
	v_mfma_i32_16x16x64_i8 v[102:105], v[142:145], v[174:177], v[102:105]
	v_mfma_i32_16x16x64_i8 v[98:101], v[150:153], v[174:177], v[98:101]
	v_mfma_i32_16x16x64_i8 v[94:97], v[142:145], v[182:185], v[94:97]
	v_mfma_i32_16x16x64_i8 v[90:93], v[150:153], v[182:185], v[90:93]
	v_mfma_i32_16x16x64_i8 v[86:89], v[142:145], v[190:193], v[86:89]
	v_mfma_i32_16x16x64_i8 v[82:85], v[150:153], v[190:193], v[82:85]
	v_mfma_i32_16x16x64_i8 v[70:73], v[142:145], v[198:201], v[70:73]
	v_mfma_i32_16x16x64_i8 v[66:69], v[150:153], v[198:201], v[66:69]
	s_setprio 0
	s_setprio 1
	v_mfma_i32_16x16x64_i8 v[30:33], v[154:157], v[170:173], v[30:33]
	v_mfma_i32_16x16x64_i8 v[26:29], v[162:165], v[170:173], v[26:29]
	v_mfma_i32_16x16x64_i8 v[22:25], v[154:157], v[178:181], v[22:25]
	v_mfma_i32_16x16x64_i8 v[18:21], v[162:165], v[178:181], v[18:21]
	v_mfma_i32_16x16x64_i8 v[14:17], v[154:157], v[186:189], v[14:17]
	v_mfma_i32_16x16x64_i8 v[10:13], v[162:165], v[186:189], v[10:13]
	v_mfma_i32_16x16x64_i8 v[6:9], v[154:157], v[194:197], v[6:9]
	v_mfma_i32_16x16x64_i8 v[2:5], v[162:165], v[194:197], v[2:5]
	v_mfma_i32_16x16x64_i8 v[30:33], v[158:161], v[174:177], v[30:33]
	v_mfma_i32_16x16x64_i8 v[26:29], v[166:169], v[174:177], v[26:29]
	v_mfma_i32_16x16x64_i8 v[22:25], v[158:161], v[182:185], v[22:25]
	v_mfma_i32_16x16x64_i8 v[18:21], v[166:169], v[182:185], v[18:21]
	v_mfma_i32_16x16x64_i8 v[14:17], v[158:161], v[190:193], v[14:17]
	v_mfma_i32_16x16x64_i8 v[10:13], v[166:169], v[190:193], v[10:13]
	v_mfma_i32_16x16x64_i8 v[6:9], v[158:161], v[198:201], v[6:9]
	v_mfma_i32_16x16x64_i8 v[2:5], v[166:169], v[198:201], v[2:5]
	s_setprio 0
	s_barrier
	s_add_i32 s28, 0, 0x18000
	v_add_u32_e32 v0, s28, v38
	s_add_i32 s29, 0, 0x1c000
	ds_read_b128 v[138:141], v0
	ds_read_b128 v[142:145], v0 offset:1024
	ds_read_b128 v[146:149], v0 offset:2048
	ds_read_b128 v[150:153], v0 offset:3072
	v_add_u32_e32 v0, s29, v38
	ds_read_b128 v[154:157], v0
	ds_read_b128 v[158:161], v0 offset:1024
	ds_read_b128 v[162:165], v0 offset:2048
	ds_read_b128 v[166:169], v0 offset:3072
	s_add_u32 s26, s12, 0x20000
	ds_read_b128 v[170:173], v39 offset:32768
	ds_read_b128 v[174:177], v39 offset:33792
	ds_read_b128 v[178:181], v39 offset:34816
	ds_read_b128 v[182:185], v39 offset:35840
	ds_read_b128 v[186:189], v39 offset:36864
	ds_read_b128 v[190:193], v39 offset:37888
	ds_read_b128 v[194:197], v39 offset:38912
	ds_read_b128 v[198:201], v39 offset:39936
	s_addc_u32 s27, s13, 0
	s_mov_b32 m0, s85
	s_nop 0
	global_load_lds_dwordx4 v34, s[12:13]
	s_mov_b32 m0, s3
	s_nop 0
	global_load_lds_dwordx4 v36, s[12:13]
	s_mov_b32 m0, s17
	s_nop 0
	global_load_lds_dwordx4 v34, s[26:27]
	s_mov_b32 m0, s18
	s_nop 0
	global_load_lds_dwordx4 v36, s[26:27]
	s_waitcnt vmcnt(8)
	s_waitcnt lgkmcnt(0)
	s_barrier
	s_setprio 1
	s_waitcnt lgkmcnt(0)
	v_mfma_i32_16x16x64_i8 v[134:137], v[138:141], v[170:173], v[134:137]
	v_mfma_i32_16x16x64_i8 v[130:133], v[146:149], v[170:173], v[130:133]
	v_mfma_i32_16x16x64_i8 v[126:129], v[138:141], v[178:181], v[126:129]
	v_mfma_i32_16x16x64_i8 v[122:125], v[146:149], v[178:181], v[122:125]
	v_mfma_i32_16x16x64_i8 v[118:121], v[138:141], v[186:189], v[118:121]
	v_mfma_i32_16x16x64_i8 v[114:117], v[146:149], v[186:189], v[114:117]
	v_mfma_i32_16x16x64_i8 v[110:113], v[138:141], v[194:197], v[110:113]
	v_mfma_i32_16x16x64_i8 v[106:109], v[146:149], v[194:197], v[106:109]
	v_mfma_i32_16x16x64_i8 v[134:137], v[142:145], v[174:177], v[134:137]
	v_mfma_i32_16x16x64_i8 v[130:133], v[150:153], v[174:177], v[130:133]
	v_mfma_i32_16x16x64_i8 v[126:129], v[142:145], v[182:185], v[126:129]
	v_mfma_i32_16x16x64_i8 v[122:125], v[150:153], v[182:185], v[122:125]
	v_mfma_i32_16x16x64_i8 v[118:121], v[142:145], v[190:193], v[118:121]
	v_mfma_i32_16x16x64_i8 v[114:117], v[150:153], v[190:193], v[114:117]
	v_mfma_i32_16x16x64_i8 v[110:113], v[142:145], v[198:201], v[110:113]
	v_mfma_i32_16x16x64_i8 v[106:109], v[150:153], v[198:201], v[106:109]
	s_setprio 0
	s_setprio 1
	v_mfma_i32_16x16x64_i8 v[78:81], v[154:157], v[170:173], v[78:81]
	v_mfma_i32_16x16x64_i8 v[74:77], v[162:165], v[170:173], v[74:77]
	v_mfma_i32_16x16x64_i8 v[62:65], v[154:157], v[178:181], v[62:65]
	v_mfma_i32_16x16x64_i8 v[58:61], v[162:165], v[178:181], v[58:61]
	v_mfma_i32_16x16x64_i8 v[54:57], v[154:157], v[186:189], v[54:57]
	v_mfma_i32_16x16x64_i8 v[50:53], v[162:165], v[186:189], v[50:53]
	v_mfma_i32_16x16x64_i8 v[44:47], v[154:157], v[194:197], v[46:49]
	v_mfma_i32_16x16x64_i8 v[40:43], v[162:165], v[194:197], v[40:43]
	v_mfma_i32_16x16x64_i8 v[78:81], v[158:161], v[174:177], v[78:81]
	v_mfma_i32_16x16x64_i8 v[74:77], v[166:169], v[174:177], v[74:77]
	v_mfma_i32_16x16x64_i8 v[62:65], v[158:161], v[182:185], v[62:65]
	v_mfma_i32_16x16x64_i8 v[58:61], v[166:169], v[182:185], v[58:61]
	v_mfma_i32_16x16x64_i8 v[54:57], v[158:161], v[190:193], v[54:57]
	v_mfma_i32_16x16x64_i8 v[50:53], v[166:169], v[190:193], v[50:53]
	v_mfma_i32_16x16x64_i8 v[46:49], v[158:161], v[198:201], v[44:47]
	v_mfma_i32_16x16x64_i8 v[42:45], v[166:169], v[198:201], v[40:43]
	s_setprio 0
	s_barrier
	v_mov_b32_e32 v0, v35
	ds_read_b128 v[170:173], v39 offset:49152
	ds_read_b128 v[174:177], v39 offset:50176
	ds_read_b128 v[178:181], v39 offset:51200
	ds_read_b128 v[182:185], v39 offset:52224
	ds_read_b128 v[186:189], v39 offset:53248
	ds_read_b128 v[190:193], v39 offset:54272
	ds_read_b128 v[194:197], v39 offset:55296
	ds_read_b128 v[198:201], v39 offset:56320
	s_add_i32 s26, s28, s33
	v_lshl_add_u64 v[40:41], s[14:15], 0, v[0:1]
	v_lshl_add_u64 v[40:41], v[40:41], 0, s[90:91]
	s_mov_b32 m0, s26
	v_mov_b32_e32 v0, v37
	global_load_lds_dwordx4 v[40:41], off
	s_add_i32 m0, s26, 0x2000
	s_nop 0
	v_lshl_add_u64 v[40:41], s[14:15], 0, v[0:1]
	s_add_u32 s14, s14, 0x20080
	v_lshl_add_u64 v[40:41], v[40:41], 0, s[90:91]
	s_addc_u32 s15, s15, 0
	s_add_i32 s26, s29, s33
	global_load_lds_dwordx4 v[40:41], off
	s_mov_b32 m0, s26
	s_nop 0
	global_load_lds_dwordx4 v35, s[14:15]
	s_add_i32 m0, s26, 0x2000
	s_nop 0
	global_load_lds_dwordx4 v37, s[14:15]
	s_waitcnt vmcnt(6)
	s_waitcnt lgkmcnt(0)
	s_barrier
	s_setprio 1
	s_waitcnt lgkmcnt(0)
	v_mfma_i32_16x16x64_i8 v[102:105], v[138:141], v[170:173], v[102:105]
	v_mfma_i32_16x16x64_i8 v[98:101], v[146:149], v[170:173], v[98:101]
	v_mfma_i32_16x16x64_i8 v[94:97], v[138:141], v[178:181], v[94:97]
	v_mfma_i32_16x16x64_i8 v[90:93], v[146:149], v[178:181], v[90:93]
	v_mfma_i32_16x16x64_i8 v[86:89], v[138:141], v[186:189], v[86:89]
	v_mfma_i32_16x16x64_i8 v[82:85], v[146:149], v[186:189], v[82:85]
	v_mfma_i32_16x16x64_i8 v[70:73], v[138:141], v[194:197], v[70:73]
	v_mfma_i32_16x16x64_i8 v[66:69], v[146:149], v[194:197], v[66:69]
	v_mfma_i32_16x16x64_i8 v[102:105], v[142:145], v[174:177], v[102:105]
	v_mfma_i32_16x16x64_i8 v[98:101], v[150:153], v[174:177], v[98:101]
	v_mfma_i32_16x16x64_i8 v[94:97], v[142:145], v[182:185], v[94:97]
	v_mfma_i32_16x16x64_i8 v[90:93], v[150:153], v[182:185], v[90:93]
	v_mfma_i32_16x16x64_i8 v[86:89], v[142:145], v[190:193], v[86:89]
	v_mfma_i32_16x16x64_i8 v[82:85], v[150:153], v[190:193], v[82:85]
	v_mfma_i32_16x16x64_i8 v[70:73], v[142:145], v[198:201], v[70:73]
	v_mfma_i32_16x16x64_i8 v[66:69], v[150:153], v[198:201], v[66:69]
	s_setprio 0
	s_setprio 1
	v_mfma_i32_16x16x64_i8 v[30:33], v[154:157], v[170:173], v[30:33]
	v_mfma_i32_16x16x64_i8 v[26:29], v[162:165], v[170:173], v[26:29]
	v_mfma_i32_16x16x64_i8 v[22:25], v[154:157], v[178:181], v[22:25]
	v_mfma_i32_16x16x64_i8 v[18:21], v[162:165], v[178:181], v[18:21]
	v_mfma_i32_16x16x64_i8 v[14:17], v[154:157], v[186:189], v[14:17]
	v_mfma_i32_16x16x64_i8 v[10:13], v[162:165], v[186:189], v[10:13]
	v_mfma_i32_16x16x64_i8 v[6:9], v[154:157], v[194:197], v[6:9]
	v_mfma_i32_16x16x64_i8 v[2:5], v[162:165], v[194:197], v[2:5]
	v_mfma_i32_16x16x64_i8 v[30:33], v[158:161], v[174:177], v[30:33]
	v_mfma_i32_16x16x64_i8 v[26:29], v[166:169], v[174:177], v[26:29]
	v_mfma_i32_16x16x64_i8 v[22:25], v[158:161], v[182:185], v[22:25]
	v_mfma_i32_16x16x64_i8 v[18:21], v[166:169], v[182:185], v[18:21]
	v_mfma_i32_16x16x64_i8 v[14:17], v[158:161], v[190:193], v[14:17]
	v_mfma_i32_16x16x64_i8 v[10:13], v[166:169], v[190:193], v[10:13]
	v_mfma_i32_16x16x64_i8 v[6:9], v[158:161], v[198:201], v[6:9]
	v_mfma_i32_16x16x64_i8 v[2:5], v[166:169], v[198:201], v[2:5]
	s_setprio 0
	s_barrier
	v_mov_b32_e32 v0, v34
	s_mov_b32 m0, s19
	v_lshl_add_u64 v[40:41], s[12:13], 0, v[0:1]
	v_lshl_add_u64 v[40:41], v[40:41], 0, s[90:91]
	v_mov_b32_e32 v0, v36
	global_load_lds_dwordx4 v[40:41], off
	s_mov_b32 m0, s20
	v_lshl_add_u64 v[40:41], s[12:13], 0, v[0:1]
	v_lshl_add_u64 v[40:41], v[40:41], 0, s[90:91]
	global_load_lds_dwordx4 v[40:41], off
	s_add_i32 s25, s25, 2
	s_add_u32 s10, s10, 0x100
	s_addc_u32 s11, s11, 0
	s_cmp_gt_u32 s25, 5
	s_cbranch_scc0 .LBB0_689
	v_readlane_b32 s6, v254, 19
	v_readlane_b32 s7, v254, 20
	s_and_b64 vcc, exec, s[6:7]
	s_cbranch_vccz .LBB0_692
	s_barrier

.LBB0_775:
	s_add_u32 s28, s8, 0xfffe0080
	s_addc_u32 s29, s9, -1
	s_add_i32 s43, 0, 0x10000
	s_cmp_eq_u32 s68, 4
	s_cselect_b32 s29, s3, s29
	s_cselect_b32 s28, s2, s28
	v_add_u32_e32 v0, s43, v198
	s_cselect_b32 s31, s64, s67
	s_cselect_b32 s30, s65, s66
	s_add_i32 s44, 0, 0x14000
	ds_read_b128 v[114:117], v0
	ds_read_b128 v[118:121], v0 offset:1024
	ds_read_b128 v[138:141], v0 offset:2048
	ds_read_b128 v[142:145], v0 offset:3072
	v_add_u32_e32 v0, s44, v198
	ds_read_b128 v[146:149], v0
	ds_read_b128 v[150:153], v0 offset:1024
	ds_read_b128 v[154:157], v0 offset:2048
	ds_read_b128 v[158:161], v0 offset:3072
	s_add_i32 s45, s85, 0xc000
	ds_read_b128 v[162:165], v199
	ds_read_b128 v[166:169], v199 offset:1024
	ds_read_b128 v[170:173], v199 offset:2048
	ds_read_b128 v[174:177], v199 offset:3072
	ds_read_b128 v[178:181], v199 offset:4096
	ds_read_b128 v[182:185], v199 offset:5120
	ds_read_b128 v[186:189], v199 offset:6144
	ds_read_b128 v[190:193], v199 offset:7168
	s_mov_b32 m0, s45
	s_add_i32 s46, s85, 0xe000
	global_load_lds_dwordx4 v194, s[8:9]
	s_mov_b32 m0, s46
	s_nop 0
	global_load_lds_dwordx4 v196, s[8:9]
	s_waitcnt vmcnt(8)
	s_waitcnt lgkmcnt(0)
	s_barrier
	s_setprio 1
	s_waitcnt lgkmcnt(0)
	v_mfma_i32_16x16x64_i8 v[134:137], v[114:117], v[162:165], v[134:137]
	v_mfma_i32_16x16x64_i8 v[130:133], v[138:141], v[162:165], v[130:133]
	v_mfma_i32_16x16x64_i8 v[126:129], v[114:117], v[170:173], v[126:129]
	v_mfma_i32_16x16x64_i8 v[122:125], v[138:141], v[170:173], v[122:125]
	v_mfma_i32_16x16x64_i8 v[110:113], v[114:117], v[178:181], v[110:113]
	v_mfma_i32_16x16x64_i8 v[106:109], v[138:141], v[178:181], v[106:109]
	v_mfma_i32_16x16x64_i8 v[102:105], v[114:117], v[186:189], v[102:105]
	v_mfma_i32_16x16x64_i8 v[98:101], v[138:141], v[186:189], v[98:101]
	v_mfma_i32_16x16x64_i8 v[134:137], v[118:121], v[166:169], v[134:137]
	v_mfma_i32_16x16x64_i8 v[130:133], v[142:145], v[166:169], v[130:133]
	v_mfma_i32_16x16x64_i8 v[126:129], v[118:121], v[174:177], v[126:129]
	v_mfma_i32_16x16x64_i8 v[122:125], v[142:145], v[174:177], v[122:125]
	v_mfma_i32_16x16x64_i8 v[110:113], v[118:121], v[182:185], v[110:113]
	v_mfma_i32_16x16x64_i8 v[106:109], v[142:145], v[182:185], v[106:109]
	v_mfma_i32_16x16x64_i8 v[102:105], v[118:121], v[190:193], v[102:105]
	v_mfma_i32_16x16x64_i8 v[98:101], v[142:145], v[190:193], v[98:101]
	s_setprio 0
	s_setprio 1
	v_mfma_i32_16x16x64_i8 v[62:65], v[146:149], v[162:165], v[62:65]
	v_mfma_i32_16x16x64_i8 v[58:61], v[154:157], v[162:165], v[58:61]
	v_mfma_i32_16x16x64_i8 v[54:57], v[146:149], v[170:173], v[54:57]
	v_mfma_i32_16x16x64_i8 v[50:53], v[154:157], v[170:173], v[50:53]
	v_mfma_i32_16x16x64_i8 v[46:49], v[146:149], v[178:181], v[46:49]
	v_mfma_i32_16x16x64_i8 v[42:45], v[154:157], v[178:181], v[42:45]
	v_mfma_i32_16x16x64_i8 v[38:41], v[146:149], v[186:189], v[38:41]
	v_mfma_i32_16x16x64_i8 v[34:37], v[154:157], v[186:189], v[34:37]
	v_mfma_i32_16x16x64_i8 v[62:65], v[150:153], v[166:169], v[62:65]
	v_mfma_i32_16x16x64_i8 v[58:61], v[158:161], v[166:169], v[58:61]
	v_mfma_i32_16x16x64_i8 v[54:57], v[150:153], v[174:177], v[54:57]
	v_mfma_i32_16x16x64_i8 v[50:53], v[158:161], v[174:177], v[50:53]
	v_mfma_i32_16x16x64_i8 v[46:49], v[150:153], v[182:185], v[46:49]
	v_mfma_i32_16x16x64_i8 v[42:45], v[158:161], v[182:185], v[42:45]
	v_mfma_i32_16x16x64_i8 v[38:41], v[150:153], v[190:193], v[38:41]
	v_mfma_i32_16x16x64_i8 v[34:37], v[158:161], v[190:193], v[34:37]
	s_setprio 0
	s_barrier
	s_add_i32 s47, s43, s33
	ds_read_b128 v[162:165], v199 offset:16384
	ds_read_b128 v[166:169], v199 offset:17408
	ds_read_b128 v[170:173], v199 offset:18432
	ds_read_b128 v[174:177], v199 offset:19456
	ds_read_b128 v[178:181], v199 offset:20480
	ds_read_b128 v[182:185], v199 offset:21504
	ds_read_b128 v[186:189], v199 offset:22528
	ds_read_b128 v[190:193], v199 offset:23552
	s_mov_b32 m0, s47
	s_add_i32 s48, s47, 0x2000
	global_load_lds_dwordx4 v195, s[30:31]
	s_mov_b32 m0, s48
	s_add_u32 s52, s30, 0x20000
	global_load_lds_dwordx4 v197, s[30:31]
	s_addc_u32 s53, s31, 0
	s_add_i32 s49, s44, s33
	s_mov_b32 m0, s49
	s_add_i32 s50, s49, 0x2000
	global_load_lds_dwordx4 v195, s[52:53]
	s_mov_b32 m0, s50
	s_nop 0
	global_load_lds_dwordx4 v197, s[52:53]
	s_waitcnt vmcnt(6)
	s_waitcnt lgkmcnt(0)
	s_barrier
	s_setprio 1
	s_waitcnt lgkmcnt(0)
	v_mfma_i32_16x16x64_i8 v[94:97], v[114:117], v[162:165], v[94:97]
	v_mfma_i32_16x16x64_i8 v[90:93], v[138:141], v[162:165], v[90:93]
	v_mfma_i32_16x16x64_i8 v[86:89], v[114:117], v[170:173], v[86:89]
	v_mfma_i32_16x16x64_i8 v[82:85], v[138:141], v[170:173], v[82:85]
	v_mfma_i32_16x16x64_i8 v[78:81], v[114:117], v[178:181], v[78:81]
	v_mfma_i32_16x16x64_i8 v[74:77], v[138:141], v[178:181], v[74:77]
	v_mfma_i32_16x16x64_i8 v[70:73], v[114:117], v[186:189], v[70:73]
	v_mfma_i32_16x16x64_i8 v[66:69], v[138:141], v[186:189], v[66:69]
	v_mfma_i32_16x16x64_i8 v[94:97], v[118:121], v[166:169], v[94:97]
	v_mfma_i32_16x16x64_i8 v[90:93], v[142:145], v[166:169], v[90:93]
	v_mfma_i32_16x16x64_i8 v[86:89], v[118:121], v[174:177], v[86:89]
	v_mfma_i32_16x16x64_i8 v[82:85], v[142:145], v[174:177], v[82:85]
	v_mfma_i32_16x16x64_i8 v[78:81], v[118:121], v[182:185], v[78:81]
	v_mfma_i32_16x16x64_i8 v[74:77], v[142:145], v[182:185], v[74:77]
	v_mfma_i32_16x16x64_i8 v[70:73], v[118:121], v[190:193], v[70:73]
	v_mfma_i32_16x16x64_i8 v[66:69], v[142:145], v[190:193], v[66:69]
	s_setprio 0
	s_setprio 1
	v_mfma_i32_16x16x64_i8 v[30:33], v[146:149], v[162:165], v[30:33]
	v_mfma_i32_16x16x64_i8 v[26:29], v[154:157], v[162:165], v[26:29]
	v_mfma_i32_16x16x64_i8 v[22:25], v[146:149], v[170:173], v[22:25]
	v_mfma_i32_16x16x64_i8 v[18:21], v[154:157], v[170:173], v[18:21]
	v_mfma_i32_16x16x64_i8 v[14:17], v[146:149], v[178:181], v[14:17]
	v_mfma_i32_16x16x64_i8 v[10:13], v[154:157], v[178:181], v[10:13]
	v_mfma_i32_16x16x64_i8 v[6:9], v[146:149], v[186:189], v[6:9]
	v_mfma_i32_16x16x64_i8 v[2:5], v[154:157], v[186:189], v[2:5]
	v_mfma_i32_16x16x64_i8 v[30:33], v[150:153], v[166:169], v[30:33]
	v_mfma_i32_16x16x64_i8 v[26:29], v[158:161], v[166:169], v[26:29]
	v_mfma_i32_16x16x64_i8 v[22:25], v[150:153], v[174:177], v[22:25]
	v_mfma_i32_16x16x64_i8 v[18:21], v[158:161], v[174:177], v[18:21]
	v_mfma_i32_16x16x64_i8 v[14:17], v[150:153], v[182:185], v[14:17]
	v_mfma_i32_16x16x64_i8 v[10:13], v[158:161], v[182:185], v[10:13]
	v_mfma_i32_16x16x64_i8 v[6:9], v[150:153], v[190:193], v[6:9]
	v_mfma_i32_16x16x64_i8 v[2:5], v[158:161], v[190:193], v[2:5]
	s_setprio 0
	s_barrier
	s_add_i32 s51, 0, 0x18000
	v_add_u32_e32 v0, s51, v198
	s_add_i32 s52, 0, 0x1c000
	ds_read_b128 v[114:117], v0
	ds_read_b128 v[118:121], v0 offset:1024
	ds_read_b128 v[138:141], v0 offset:2048
	ds_read_b128 v[142:145], v0 offset:3072
	v_add_u32_e32 v0, s52, v198
	ds_read_b128 v[146:149], v0
	ds_read_b128 v[150:153], v0 offset:1024
	ds_read_b128 v[154:157], v0 offset:2048
	ds_read_b128 v[158:161], v0 offset:3072
	s_add_u32 s54, s28, 0x20000
	ds_read_b128 v[162:165], v199 offset:32768
	ds_read_b128 v[166:169], v199 offset:33792
	ds_read_b128 v[170:173], v199 offset:34816
	ds_read_b128 v[174:177], v199 offset:35840
	ds_read_b128 v[178:181], v199 offset:36864
	ds_read_b128 v[182:185], v199 offset:37888
	ds_read_b128 v[186:189], v199 offset:38912
	ds_read_b128 v[190:193], v199 offset:39936
	s_addc_u32 s55, s29, 0
	s_mov_b32 m0, s85
	s_nop 0
	global_load_lds_dwordx4 v194, s[28:29]
	s_mov_b32 m0, s38
	s_nop 0
	global_load_lds_dwordx4 v196, s[28:29]
	s_mov_b32 m0, s39
	s_nop 0
	global_load_lds_dwordx4 v194, s[54:55]
	s_mov_b32 m0, s40
	s_nop 0
	global_load_lds_dwordx4 v196, s[54:55]
	s_waitcnt vmcnt(8)
	s_waitcnt lgkmcnt(0)
	s_barrier
	s_setprio 1
	s_waitcnt lgkmcnt(0)
	v_mfma_i32_16x16x64_i8 v[134:137], v[114:117], v[162:165], v[134:137]
	v_mfma_i32_16x16x64_i8 v[130:133], v[138:141], v[162:165], v[130:133]
	v_mfma_i32_16x16x64_i8 v[126:129], v[114:117], v[170:173], v[126:129]
	v_mfma_i32_16x16x64_i8 v[122:125], v[138:141], v[170:173], v[122:125]
	v_mfma_i32_16x16x64_i8 v[110:113], v[114:117], v[178:181], v[110:113]
	v_mfma_i32_16x16x64_i8 v[106:109], v[138:141], v[178:181], v[106:109]
	v_mfma_i32_16x16x64_i8 v[102:105], v[114:117], v[186:189], v[102:105]
	v_mfma_i32_16x16x64_i8 v[98:101], v[138:141], v[186:189], v[98:101]
	v_mfma_i32_16x16x64_i8 v[134:137], v[118:121], v[166:169], v[134:137]
	v_mfma_i32_16x16x64_i8 v[130:133], v[142:145], v[166:169], v[130:133]
	v_mfma_i32_16x16x64_i8 v[126:129], v[118:121], v[174:177], v[126:129]
	v_mfma_i32_16x16x64_i8 v[122:125], v[142:145], v[174:177], v[122:125]
	v_mfma_i32_16x16x64_i8 v[110:113], v[118:121], v[182:185], v[110:113]
	v_mfma_i32_16x16x64_i8 v[106:109], v[142:145], v[182:185], v[106:109]
	v_mfma_i32_16x16x64_i8 v[102:105], v[118:121], v[190:193], v[102:105]
	v_mfma_i32_16x16x64_i8 v[98:101], v[142:145], v[190:193], v[98:101]
	s_setprio 0
	s_setprio 1
	v_mfma_i32_16x16x64_i8 v[62:65], v[146:149], v[162:165], v[62:65]
	v_mfma_i32_16x16x64_i8 v[58:61], v[154:157], v[162:165], v[58:61]
	v_mfma_i32_16x16x64_i8 v[54:57], v[146:149], v[170:173], v[54:57]
	v_mfma_i32_16x16x64_i8 v[50:53], v[154:157], v[170:173], v[50:53]
	v_mfma_i32_16x16x64_i8 v[46:49], v[146:149], v[178:181], v[46:49]
	v_mfma_i32_16x16x64_i8 v[42:45], v[154:157], v[178:181], v[42:45]
	v_mfma_i32_16x16x64_i8 v[38:41], v[146:149], v[186:189], v[38:41]
	v_mfma_i32_16x16x64_i8 v[34:37], v[154:157], v[186:189], v[34:37]
	v_mfma_i32_16x16x64_i8 v[62:65], v[150:153], v[166:169], v[62:65]
	v_mfma_i32_16x16x64_i8 v[58:61], v[158:161], v[166:169], v[58:61]
	v_mfma_i32_16x16x64_i8 v[54:57], v[150:153], v[174:177], v[54:57]
	v_mfma_i32_16x16x64_i8 v[50:53], v[158:161], v[174:177], v[50:53]
	v_mfma_i32_16x16x64_i8 v[46:49], v[150:153], v[182:185], v[46:49]
	v_mfma_i32_16x16x64_i8 v[42:45], v[158:161], v[182:185], v[42:45]
	v_mfma_i32_16x16x64_i8 v[38:41], v[150:153], v[190:193], v[38:41]
	v_mfma_i32_16x16x64_i8 v[34:37], v[158:161], v[190:193], v[34:37]
	s_setprio 0
	s_barrier
	v_mov_b32_e32 v0, v195
	ds_read_b128 v[162:165], v199 offset:49152
	ds_read_b128 v[166:169], v199 offset:50176
	ds_read_b128 v[170:173], v199 offset:51200
	ds_read_b128 v[174:177], v199 offset:52224
	ds_read_b128 v[178:181], v199 offset:53248
	ds_read_b128 v[182:185], v199 offset:54272
	ds_read_b128 v[186:189], v199 offset:55296
	ds_read_b128 v[190:193], v199 offset:56320
	s_add_i32 s53, s51, s33
	v_lshl_add_u64 v[200:201], s[30:31], 0, v[0:1]
	v_lshl_add_u64 v[200:201], v[200:201], 0, s[90:91]
	s_mov_b32 m0, s53
	v_mov_b32_e32 v0, v197
	s_add_i32 s54, s53, 0x2000
	global_load_lds_dwordx4 v[200:201], off
	s_mov_b32 m0, s54
	v_lshl_add_u64 v[200:201], s[30:31], 0, v[0:1]
	s_add_u32 s30, s30, 0x20080
	v_lshl_add_u64 v[200:201], v[200:201], 0, s[90:91]
	s_addc_u32 s31, s31, 0
	s_add_i32 s55, s52, s33
	global_load_lds_dwordx4 v[200:201], off
	s_mov_b32 m0, s55
	s_add_i32 s56, s55, 0x2000
	global_load_lds_dwordx4 v195, s[30:31]
	s_mov_b32 m0, s56
	s_nop 0
	global_load_lds_dwordx4 v197, s[30:31]
	s_waitcnt vmcnt(6)
	s_waitcnt lgkmcnt(0)
	s_barrier
	s_setprio 1
	s_waitcnt lgkmcnt(0)
	v_mfma_i32_16x16x64_i8 v[94:97], v[114:117], v[162:165], v[94:97]
	v_mfma_i32_16x16x64_i8 v[90:93], v[138:141], v[162:165], v[90:93]
	v_mfma_i32_16x16x64_i8 v[86:89], v[114:117], v[170:173], v[86:89]
	v_mfma_i32_16x16x64_i8 v[82:85], v[138:141], v[170:173], v[82:85]
	v_mfma_i32_16x16x64_i8 v[78:81], v[114:117], v[178:181], v[78:81]
	v_mfma_i32_16x16x64_i8 v[74:77], v[138:141], v[178:181], v[74:77]
	v_mfma_i32_16x16x64_i8 v[70:73], v[114:117], v[186:189], v[70:73]
	v_mfma_i32_16x16x64_i8 v[66:69], v[138:141], v[186:189], v[66:69]
	v_mfma_i32_16x16x64_i8 v[94:97], v[118:121], v[166:169], v[94:97]
	v_mfma_i32_16x16x64_i8 v[90:93], v[142:145], v[166:169], v[90:93]
	v_mfma_i32_16x16x64_i8 v[86:89], v[118:121], v[174:177], v[86:89]
	v_mfma_i32_16x16x64_i8 v[82:85], v[142:145], v[174:177], v[82:85]
	v_mfma_i32_16x16x64_i8 v[78:81], v[118:121], v[182:185], v[78:81]
	v_mfma_i32_16x16x64_i8 v[74:77], v[142:145], v[182:185], v[74:77]
	v_mfma_i32_16x16x64_i8 v[70:73], v[118:121], v[190:193], v[70:73]
	v_mfma_i32_16x16x64_i8 v[66:69], v[142:145], v[190:193], v[66:69]
	s_setprio 0
	s_setprio 1
	v_mfma_i32_16x16x64_i8 v[30:33], v[146:149], v[162:165], v[30:33]
	v_mfma_i32_16x16x64_i8 v[26:29], v[154:157], v[162:165], v[26:29]
	v_mfma_i32_16x16x64_i8 v[22:25], v[146:149], v[170:173], v[22:25]
	v_mfma_i32_16x16x64_i8 v[18:21], v[154:157], v[170:173], v[18:21]
	v_mfma_i32_16x16x64_i8 v[14:17], v[146:149], v[178:181], v[14:17]
	v_mfma_i32_16x16x64_i8 v[10:13], v[154:157], v[178:181], v[10:13]
	v_mfma_i32_16x16x64_i8 v[6:9], v[146:149], v[186:189], v[6:9]
	v_mfma_i32_16x16x64_i8 v[2:5], v[154:157], v[186:189], v[2:5]
	v_mfma_i32_16x16x64_i8 v[30:33], v[150:153], v[166:169], v[30:33]
	v_mfma_i32_16x16x64_i8 v[26:29], v[158:161], v[166:169], v[26:29]
	v_mfma_i32_16x16x64_i8 v[22:25], v[150:153], v[174:177], v[22:25]
	v_mfma_i32_16x16x64_i8 v[18:21], v[158:161], v[174:177], v[18:21]
	v_mfma_i32_16x16x64_i8 v[14:17], v[150:153], v[182:185], v[14:17]
	v_mfma_i32_16x16x64_i8 v[10:13], v[158:161], v[182:185], v[10:13]
	v_mfma_i32_16x16x64_i8 v[6:9], v[150:153], v[190:193], v[6:9]
	v_mfma_i32_16x16x64_i8 v[2:5], v[158:161], v[190:193], v[2:5]
	s_setprio 0
	s_barrier
	v_mov_b32_e32 v0, v194
	s_mov_b32 m0, s41
	v_lshl_add_u64 v[192:193], s[28:29], 0, v[0:1]
	v_lshl_add_u64 v[192:193], v[192:193], 0, s[90:91]
	v_mov_b32_e32 v0, v196
	global_load_lds_dwordx4 v[192:193], off
	s_mov_b32 m0, s42
	v_lshl_add_u64 v[192:193], s[28:29], 0, v[0:1]
	v_lshl_add_u64 v[192:193], v[192:193], 0, s[90:91]
	global_load_lds_dwordx4 v[192:193], off
	s_add_i32 s68, s68, 2
	s_add_u32 s8, s8, 0x100
	s_addc_u32 s9, s9, 0
	s_add_u32 s66, s66, 0x100
	s_addc_u32 s67, s67, 0
	s_cmp_gt_u32 s68, 5
	s_cbranch_scc0 .LBB0_775
	v_readlane_b32 s8, v254, 19
	v_readlane_b32 s9, v254, 20
	s_and_b64 vcc, exec, s[8:9]
	s_cbranch_vccz .LBB0_778
	s_barrier

.LBB0_866:
	v_add_u32_e32 v0, s43, v248
	ds_read_b128 v[66:69], v0
	ds_read_b128 v[70:73], v0 offset:1024
	ds_read_b128 v[82:85], v0 offset:2048
	ds_read_b128 v[86:89], v0 offset:3072
	v_add_u32_e32 v0, s44, v248
	ds_read_b128 v[106:109], v0
	ds_read_b128 v[110:113], v0 offset:1024
	ds_read_b128 v[122:125], v0 offset:2048
	ds_read_b128 v[130:133], v0 offset:3072
	s_add_u32 s12, s10, 0xfff70080
	s_addc_u32 s13, s11, -1
	s_cmp_eq_u32 s66, 2
	s_cselect_b32 s13, s27, s13
	s_cselect_b32 s12, s26, s12
	s_cselect_b32 s15, s25, s65
	s_cselect_b32 s14, s24, s29
	s_mov_b32 m0, s45
	ds_read_b128 v[162:165], v249
	ds_read_b128 v[166:169], v249 offset:1024
	ds_read_b128 v[170:173], v249 offset:2048
	ds_read_b128 v[174:177], v249 offset:3072
	ds_read_b128 v[178:181], v249 offset:4096
	ds_read_b128 v[182:185], v249 offset:5120
	ds_read_b128 v[186:189], v249 offset:6144
	ds_read_b128 v[190:193], v249 offset:7168
	s_nop 0
	global_load_lds_dwordx4 v244, s[10:11]
	s_mov_b32 m0, s46
	s_nop 0
	global_load_lds_dwordx4 v246, s[10:11]
	s_waitcnt vmcnt(8)
	s_waitcnt lgkmcnt(0)
	s_barrier
	s_setprio 1
	s_waitcnt lgkmcnt(0)
	v_mfma_f32_16x16x32_bf16 v[158:161], v[66:69], v[162:165], v[158:161]
	v_mfma_f32_16x16x32_bf16 v[154:157], v[82:85], v[162:165], v[154:157]
	v_mfma_f32_16x16x32_bf16 v[142:145], v[66:69], v[170:173], v[142:145]
	v_mfma_f32_16x16x32_bf16 v[138:141], v[82:85], v[170:173], v[138:141]
	v_mfma_f32_16x16x32_bf16 v[118:121], v[66:69], v[178:181], v[118:121]
	v_mfma_f32_16x16x32_bf16 v[114:117], v[82:85], v[178:181], v[114:117]
	v_mfma_f32_16x16x32_bf16 v[94:97], v[66:69], v[186:189], v[94:97]
	v_mfma_f32_16x16x32_bf16 v[90:93], v[82:85], v[186:189], v[90:93]
	v_mfma_f32_16x16x32_bf16 v[158:161], v[70:73], v[166:169], v[158:161]
	v_mfma_f32_16x16x32_bf16 v[154:157], v[86:89], v[166:169], v[154:157]
	v_mfma_f32_16x16x32_bf16 v[142:145], v[70:73], v[174:177], v[142:145]
	v_mfma_f32_16x16x32_bf16 v[138:141], v[86:89], v[174:177], v[138:141]
	v_mfma_f32_16x16x32_bf16 v[118:121], v[70:73], v[182:185], v[118:121]
	v_mfma_f32_16x16x32_bf16 v[114:117], v[86:89], v[182:185], v[114:117]
	v_mfma_f32_16x16x32_bf16 v[94:97], v[70:73], v[190:193], v[94:97]
	v_mfma_f32_16x16x32_bf16 v[90:93], v[86:89], v[190:193], v[90:93]
	s_setprio 0
	s_setprio 1
	v_mfma_f32_16x16x32_bf16 v[150:153], v[106:109], v[162:165], v[150:153]
	v_mfma_f32_16x16x32_bf16 v[146:149], v[122:125], v[162:165], v[146:149]
	v_mfma_f32_16x16x32_bf16 v[134:137], v[106:109], v[170:173], v[134:137]
	v_mfma_f32_16x16x32_bf16 v[126:129], v[122:125], v[170:173], v[126:129]
	v_mfma_f32_16x16x32_bf16 v[102:105], v[106:109], v[178:181], v[102:105]
	v_mfma_f32_16x16x32_bf16 v[98:101], v[122:125], v[178:181], v[98:101]
	v_mfma_f32_16x16x32_bf16 v[78:81], v[106:109], v[186:189], v[78:81]
	v_mfma_f32_16x16x32_bf16 v[74:77], v[122:125], v[186:189], v[74:77]
	v_mfma_f32_16x16x32_bf16 v[150:153], v[110:113], v[166:169], v[150:153]
	v_mfma_f32_16x16x32_bf16 v[146:149], v[130:133], v[166:169], v[146:149]
	v_mfma_f32_16x16x32_bf16 v[134:137], v[110:113], v[174:177], v[134:137]
	v_mfma_f32_16x16x32_bf16 v[126:129], v[130:133], v[174:177], v[126:129]
	v_mfma_f32_16x16x32_bf16 v[102:105], v[110:113], v[182:185], v[102:105]
	v_mfma_f32_16x16x32_bf16 v[98:101], v[130:133], v[182:185], v[98:101]
	v_mfma_f32_16x16x32_bf16 v[78:81], v[110:113], v[190:193], v[78:81]
	v_mfma_f32_16x16x32_bf16 v[74:77], v[130:133], v[190:193], v[74:77]
	s_setprio 0
	s_barrier
	s_mov_b32 m0, s47
	ds_read_b128 v[162:165], v249 offset:16384
	ds_read_b128 v[166:169], v249 offset:17408
	ds_read_b128 v[170:173], v249 offset:18432
	ds_read_b128 v[174:177], v249 offset:19456
	ds_read_b128 v[178:181], v249 offset:20480
	ds_read_b128 v[182:185], v249 offset:21504
	ds_read_b128 v[186:189], v249 offset:22528
	ds_read_b128 v[190:193], v249 offset:23552
	s_add_u32 s68, s14, 0x18000
	global_load_lds_dwordx4 v245, s[14:15]
	s_mov_b32 m0, s48
	s_addc_u32 s69, s15, 0
	global_load_lds_dwordx4 v247, s[14:15]
	s_mov_b32 m0, s49
	s_nop 0
	global_load_lds_dwordx4 v245, s[68:69]
	s_mov_b32 m0, s50
	s_nop 0
	global_load_lds_dwordx4 v247, s[68:69]
	s_waitcnt vmcnt(6)
	s_waitcnt lgkmcnt(0)
	s_barrier
	s_setprio 1
	s_waitcnt lgkmcnt(0)
	v_mfma_f32_16x16x32_bf16 v[62:65], v[66:69], v[162:165], v[62:65]
	v_mfma_f32_16x16x32_bf16 v[58:61], v[82:85], v[162:165], v[58:61]
	v_mfma_f32_16x16x32_bf16 v[46:49], v[66:69], v[170:173], v[46:49]
	v_mfma_f32_16x16x32_bf16 v[42:45], v[82:85], v[170:173], v[42:45]
	v_mfma_f32_16x16x32_bf16 v[30:33], v[66:69], v[178:181], v[30:33]
	v_mfma_f32_16x16x32_bf16 v[26:29], v[82:85], v[178:181], v[26:29]
	v_mfma_f32_16x16x32_bf16 v[14:17], v[66:69], v[186:189], v[14:17]
	v_mfma_f32_16x16x32_bf16 v[10:13], v[82:85], v[186:189], v[10:13]
	v_mfma_f32_16x16x32_bf16 v[62:65], v[70:73], v[166:169], v[62:65]
	v_mfma_f32_16x16x32_bf16 v[58:61], v[86:89], v[166:169], v[58:61]
	v_mfma_f32_16x16x32_bf16 v[46:49], v[70:73], v[174:177], v[46:49]
	v_mfma_f32_16x16x32_bf16 v[42:45], v[86:89], v[174:177], v[42:45]
	v_mfma_f32_16x16x32_bf16 v[30:33], v[70:73], v[182:185], v[30:33]
	v_mfma_f32_16x16x32_bf16 v[26:29], v[86:89], v[182:185], v[26:29]
	v_mfma_f32_16x16x32_bf16 v[14:17], v[70:73], v[190:193], v[14:17]
	v_mfma_f32_16x16x32_bf16 v[10:13], v[86:89], v[190:193], v[10:13]
	s_setprio 0
	s_setprio 1
	v_mfma_f32_16x16x32_bf16 v[54:57], v[106:109], v[162:165], v[54:57]
	v_mfma_f32_16x16x32_bf16 v[50:53], v[122:125], v[162:165], v[50:53]
	v_mfma_f32_16x16x32_bf16 v[38:41], v[106:109], v[170:173], v[38:41]
	v_mfma_f32_16x16x32_bf16 v[34:37], v[122:125], v[170:173], v[34:37]
	v_mfma_f32_16x16x32_bf16 v[22:25], v[106:109], v[178:181], v[22:25]
	v_mfma_f32_16x16x32_bf16 v[18:21], v[122:125], v[178:181], v[18:21]
	v_mfma_f32_16x16x32_bf16 v[6:9], v[106:109], v[186:189], v[6:9]
	v_mfma_f32_16x16x32_bf16 v[2:5], v[122:125], v[186:189], v[2:5]
	v_mfma_f32_16x16x32_bf16 v[54:57], v[110:113], v[166:169], v[54:57]
	v_mfma_f32_16x16x32_bf16 v[50:53], v[130:133], v[166:169], v[50:53]
	v_mfma_f32_16x16x32_bf16 v[38:41], v[110:113], v[174:177], v[38:41]
	v_mfma_f32_16x16x32_bf16 v[34:37], v[130:133], v[174:177], v[34:37]
	v_mfma_f32_16x16x32_bf16 v[22:25], v[110:113], v[182:185], v[22:25]
	v_mfma_f32_16x16x32_bf16 v[18:21], v[130:133], v[182:185], v[18:21]
	v_mfma_f32_16x16x32_bf16 v[6:9], v[110:113], v[190:193], v[6:9]
	v_mfma_f32_16x16x32_bf16 v[2:5], v[130:133], v[190:193], v[2:5]
	s_setprio 0
	s_barrier
	v_add_u32_e32 v0, s51, v248
	ds_read_b128 v[66:69], v0
	ds_read_b128 v[70:73], v0 offset:1024
	ds_read_b128 v[82:85], v0 offset:2048
	ds_read_b128 v[86:89], v0 offset:3072
	v_add_u32_e32 v0, s52, v248
	ds_read_b128 v[106:109], v0
	ds_read_b128 v[110:113], v0 offset:1024
	ds_read_b128 v[122:125], v0 offset:2048
	ds_read_b128 v[130:133], v0 offset:3072
	s_add_u32 s68, s12, 0x90000
	ds_read_b128 v[162:165], v249 offset:32768
	ds_read_b128 v[166:169], v249 offset:33792
	ds_read_b128 v[170:173], v249 offset:34816
	ds_read_b128 v[174:177], v249 offset:35840
	ds_read_b128 v[178:181], v249 offset:36864
	ds_read_b128 v[182:185], v249 offset:37888
	ds_read_b128 v[186:189], v249 offset:38912
	ds_read_b128 v[190:193], v249 offset:39936
	s_addc_u32 s69, s13, 0
	s_mov_b32 m0, s85
	s_nop 0
	global_load_lds_dwordx4 v244, s[12:13]
	s_mov_b32 m0, s38
	s_nop 0
	global_load_lds_dwordx4 v246, s[12:13]
	s_mov_b32 m0, s39
	s_nop 0
	global_load_lds_dwordx4 v244, s[68:69]
	s_mov_b32 m0, s40
	s_nop 0
	global_load_lds_dwordx4 v246, s[68:69]
	s_waitcnt vmcnt(8)
	s_waitcnt lgkmcnt(0)
	s_barrier
	s_setprio 1
	s_waitcnt lgkmcnt(0)
	v_mfma_f32_16x16x32_bf16 v[158:161], v[66:69], v[162:165], v[158:161]
	v_mfma_f32_16x16x32_bf16 v[154:157], v[82:85], v[162:165], v[154:157]
	v_mfma_f32_16x16x32_bf16 v[142:145], v[66:69], v[170:173], v[142:145]
	v_mfma_f32_16x16x32_bf16 v[138:141], v[82:85], v[170:173], v[138:141]
	v_mfma_f32_16x16x32_bf16 v[118:121], v[66:69], v[178:181], v[118:121]
	v_mfma_f32_16x16x32_bf16 v[114:117], v[82:85], v[178:181], v[114:117]
	v_mfma_f32_16x16x32_bf16 v[94:97], v[66:69], v[186:189], v[94:97]
	v_mfma_f32_16x16x32_bf16 v[90:93], v[82:85], v[186:189], v[90:93]
	v_mfma_f32_16x16x32_bf16 v[158:161], v[70:73], v[166:169], v[158:161]
	v_mfma_f32_16x16x32_bf16 v[154:157], v[86:89], v[166:169], v[154:157]
	v_mfma_f32_16x16x32_bf16 v[142:145], v[70:73], v[174:177], v[142:145]
	v_mfma_f32_16x16x32_bf16 v[138:141], v[86:89], v[174:177], v[138:141]
	v_mfma_f32_16x16x32_bf16 v[118:121], v[70:73], v[182:185], v[118:121]
	v_mfma_f32_16x16x32_bf16 v[114:117], v[86:89], v[182:185], v[114:117]
	v_mfma_f32_16x16x32_bf16 v[94:97], v[70:73], v[190:193], v[94:97]
	v_mfma_f32_16x16x32_bf16 v[90:93], v[86:89], v[190:193], v[90:93]
	s_setprio 0
	s_setprio 1
	v_mfma_f32_16x16x32_bf16 v[150:153], v[106:109], v[162:165], v[150:153]
	v_mfma_f32_16x16x32_bf16 v[146:149], v[122:125], v[162:165], v[146:149]
	v_mfma_f32_16x16x32_bf16 v[134:137], v[106:109], v[170:173], v[134:137]
	v_mfma_f32_16x16x32_bf16 v[126:129], v[122:125], v[170:173], v[126:129]
	v_mfma_f32_16x16x32_bf16 v[102:105], v[106:109], v[178:181], v[102:105]
	v_mfma_f32_16x16x32_bf16 v[98:101], v[122:125], v[178:181], v[98:101]
	v_mfma_f32_16x16x32_bf16 v[78:81], v[106:109], v[186:189], v[78:81]
	v_mfma_f32_16x16x32_bf16 v[74:77], v[122:125], v[186:189], v[74:77]
	v_mfma_f32_16x16x32_bf16 v[150:153], v[110:113], v[166:169], v[150:153]
	v_mfma_f32_16x16x32_bf16 v[146:149], v[130:133], v[166:169], v[146:149]
	v_mfma_f32_16x16x32_bf16 v[134:137], v[110:113], v[174:177], v[134:137]
	v_mfma_f32_16x16x32_bf16 v[126:129], v[130:133], v[174:177], v[126:129]
	v_mfma_f32_16x16x32_bf16 v[102:105], v[110:113], v[182:185], v[102:105]
	v_mfma_f32_16x16x32_bf16 v[98:101], v[130:133], v[182:185], v[98:101]
	v_mfma_f32_16x16x32_bf16 v[78:81], v[110:113], v[190:193], v[78:81]
	v_mfma_f32_16x16x32_bf16 v[74:77], v[130:133], v[190:193], v[74:77]
	s_setprio 0
	s_barrier
	v_mov_b32_e32 v0, v245
	ds_read_b128 v[162:165], v249 offset:49152
	ds_read_b128 v[166:169], v249 offset:50176
	ds_read_b128 v[170:173], v249 offset:51200
	ds_read_b128 v[174:177], v249 offset:52224
	ds_read_b128 v[178:181], v249 offset:53248
	ds_read_b128 v[182:185], v249 offset:54272
	ds_read_b128 v[186:189], v249 offset:55296
	ds_read_b128 v[190:193], v249 offset:56320
	s_mov_b32 m0, s53
	v_lshl_add_u64 v[194:195], s[14:15], 0, v[0:1]
	v_lshl_add_u64 v[194:195], v[194:195], 0, s[90:91]
	v_mov_b32_e32 v0, v247
	global_load_lds_dwordx4 v[194:195], off
	s_mov_b32 m0, s54
	v_lshl_add_u64 v[194:195], s[14:15], 0, v[0:1]
	v_lshl_add_u64 v[194:195], v[194:195], 0, s[90:91]
	s_add_u32 s14, s14, 0x18080
	global_load_lds_dwordx4 v[194:195], off
	s_addc_u32 s15, s15, 0
	s_mov_b32 m0, s55
	s_nop 0
	global_load_lds_dwordx4 v245, s[14:15]
	s_mov_b32 m0, s56
	s_nop 0
	global_load_lds_dwordx4 v247, s[14:15]
	s_waitcnt vmcnt(6)
	s_waitcnt lgkmcnt(0)
	s_barrier
	s_setprio 1
	s_waitcnt lgkmcnt(0)
	v_mfma_f32_16x16x32_bf16 v[62:65], v[66:69], v[162:165], v[62:65]
	v_mfma_f32_16x16x32_bf16 v[58:61], v[82:85], v[162:165], v[58:61]
	v_mfma_f32_16x16x32_bf16 v[46:49], v[66:69], v[170:173], v[46:49]
	v_mfma_f32_16x16x32_bf16 v[42:45], v[82:85], v[170:173], v[42:45]
	v_mfma_f32_16x16x32_bf16 v[30:33], v[66:69], v[178:181], v[30:33]
	v_mfma_f32_16x16x32_bf16 v[26:29], v[82:85], v[178:181], v[26:29]
	v_mfma_f32_16x16x32_bf16 v[14:17], v[66:69], v[186:189], v[14:17]
	v_mfma_f32_16x16x32_bf16 v[10:13], v[82:85], v[186:189], v[10:13]
	v_mfma_f32_16x16x32_bf16 v[62:65], v[70:73], v[166:169], v[62:65]
	v_mfma_f32_16x16x32_bf16 v[58:61], v[86:89], v[166:169], v[58:61]
	v_mfma_f32_16x16x32_bf16 v[46:49], v[70:73], v[174:177], v[46:49]
	v_mfma_f32_16x16x32_bf16 v[42:45], v[86:89], v[174:177], v[42:45]
	v_mfma_f32_16x16x32_bf16 v[30:33], v[70:73], v[182:185], v[30:33]
	v_mfma_f32_16x16x32_bf16 v[26:29], v[86:89], v[182:185], v[26:29]
	v_mfma_f32_16x16x32_bf16 v[14:17], v[70:73], v[190:193], v[14:17]
	v_mfma_f32_16x16x32_bf16 v[10:13], v[86:89], v[190:193], v[10:13]
	s_setprio 0
	s_setprio 1
	v_mfma_f32_16x16x32_bf16 v[54:57], v[106:109], v[162:165], v[54:57]
	v_mfma_f32_16x16x32_bf16 v[50:53], v[122:125], v[162:165], v[50:53]
	v_mfma_f32_16x16x32_bf16 v[38:41], v[106:109], v[170:173], v[38:41]
	v_mfma_f32_16x16x32_bf16 v[34:37], v[122:125], v[170:173], v[34:37]
	v_mfma_f32_16x16x32_bf16 v[22:25], v[106:109], v[178:181], v[22:25]
	v_mfma_f32_16x16x32_bf16 v[18:21], v[122:125], v[178:181], v[18:21]
	v_mfma_f32_16x16x32_bf16 v[6:9], v[106:109], v[186:189], v[6:9]
	v_mfma_f32_16x16x32_bf16 v[2:5], v[122:125], v[186:189], v[2:5]
	v_mfma_f32_16x16x32_bf16 v[54:57], v[110:113], v[166:169], v[54:57]
	v_mfma_f32_16x16x32_bf16 v[50:53], v[130:133], v[166:169], v[50:53]
	v_mfma_f32_16x16x32_bf16 v[38:41], v[110:113], v[174:177], v[38:41]
	v_mfma_f32_16x16x32_bf16 v[34:37], v[130:133], v[174:177], v[34:37]
	v_mfma_f32_16x16x32_bf16 v[22:25], v[110:113], v[182:185], v[22:25]
	v_mfma_f32_16x16x32_bf16 v[18:21], v[130:133], v[182:185], v[18:21]
	v_mfma_f32_16x16x32_bf16 v[6:9], v[110:113], v[190:193], v[6:9]
	v_mfma_f32_16x16x32_bf16 v[2:5], v[130:133], v[190:193], v[2:5]
	s_setprio 0
	s_barrier
	v_mov_b32_e32 v0, v244
	s_mov_b32 m0, s41
	v_lshl_add_u64 v[194:195], s[12:13], 0, v[0:1]
	v_lshl_add_u64 v[194:195], v[194:195], 0, s[90:91]
	v_mov_b32_e32 v0, v246
	global_load_lds_dwordx4 v[194:195], off
	s_mov_b32 m0, s42
	v_lshl_add_u64 v[194:195], s[12:13], 0, v[0:1]
	v_lshl_add_u64 v[194:195], v[194:195], 0, s[90:91]
	global_load_lds_dwordx4 v[194:195], off
	s_add_i32 s66, s66, 2
	s_add_u32 s10, s10, 0x100
	s_addc_u32 s11, s11, 0
	s_add_u32 s29, s29, 0x100
	s_addc_u32 s65, s65, 0
	s_cmp_gt_u32 s66, 3
	s_cbranch_scc0 .LBB0_866
	v_readlane_b32 s10, v254, 19
	v_readlane_b32 s11, v254, 20
	s_and_b64 vcc, exec, s[10:11]
	s_cbranch_vccz .LBB0_869
	s_barrier

.LBB0_918:
	s_add_u32 s30, s14, s28
	s_addc_u32 s31, s15, s29
	s_add_u32 s34, s30, 0x100
	s_addc_u32 s35, s31, 0
	s_and_b64 s[24:25], s[26:27], exec
	s_cselect_b32 s25, s11, s35
	s_cselect_b32 s24, s10, s34
	s_add_u32 s28, s20, s28
	s_addc_u32 s29, s21, s29
	s_add_u32 s28, s28, 0x100
	s_addc_u32 s29, s29, 0
	s_and_b64 s[26:27], s[26:27], exec
	v_add_u32_e32 v0, s43, v151
	s_cselect_b32 s27, s59, s29
	s_cselect_b32 s26, s65, s28
	s_add_u32 s36, s30, 0x90080
	ds_read_b128 v[130:133], v0
	ds_read_b128 v[134:137], v0 offset:1024
	ds_read_b128 v[154:157], v0 offset:2048
	ds_read_b128 v[158:161], v0 offset:3072
	v_add_u32_e32 v0, s44, v151
	s_addc_u32 s37, s31, 0
	ds_read_b128 v[162:165], v0
	ds_read_b128 v[166:169], v0 offset:1024
	ds_read_b128 v[170:173], v0 offset:2048
	ds_read_b128 v[174:177], v0 offset:3072
	s_add_u32 s34, s26, 0x10000
	s_addc_u32 s35, s27, 0
	s_add_u32 s30, s24, 0x90000
	s_addc_u32 s31, s25, 0
	s_add_u32 s28, s26, 0x10080
	s_addc_u32 s29, s27, 0
	s_mov_b32 m0, s45
	ds_read_b128 v[178:181], v152
	ds_read_b128 v[182:185], v152 offset:1024
	ds_read_b128 v[186:189], v152 offset:2048
	ds_read_b128 v[190:193], v152 offset:3072
	ds_read_b128 v[194:197], v152 offset:4096
	ds_read_b128 v[198:201], v152 offset:5120
	ds_read_b128 v[202:205], v152 offset:6144
	ds_read_b128 v[206:209], v152 offset:7168
	s_nop 0
	global_load_lds_dwordx4 v141, s[36:37]
	s_mov_b32 m0, s46
	s_nop 0
	global_load_lds_dwordx4 v149, s[36:37]
	s_waitcnt vmcnt(8)
	s_waitcnt lgkmcnt(0)
	s_barrier
	s_setprio 1
	s_waitcnt lgkmcnt(0)
	v_mfma_f32_16x16x32_bf16 v[126:129], v[130:133], v[178:181], v[126:129]
	v_mfma_f32_16x16x32_bf16 v[122:125], v[154:157], v[178:181], v[122:125]
	v_mfma_f32_16x16x32_bf16 v[118:121], v[130:133], v[186:189], v[118:121]
	v_mfma_f32_16x16x32_bf16 v[110:113], v[154:157], v[186:189], v[110:113]
	v_mfma_f32_16x16x32_bf16 v[102:105], v[130:133], v[194:197], v[102:105]
	v_mfma_f32_16x16x32_bf16 v[94:97], v[154:157], v[194:197], v[94:97]
	v_mfma_f32_16x16x32_bf16 v[86:89], v[130:133], v[202:205], v[86:89]
	v_mfma_f32_16x16x32_bf16 v[78:81], v[154:157], v[202:205], v[78:81]
	v_mfma_f32_16x16x32_bf16 v[126:129], v[134:137], v[182:185], v[126:129]
	v_mfma_f32_16x16x32_bf16 v[122:125], v[158:161], v[182:185], v[122:125]
	v_mfma_f32_16x16x32_bf16 v[118:121], v[134:137], v[190:193], v[118:121]
	v_mfma_f32_16x16x32_bf16 v[110:113], v[158:161], v[190:193], v[110:113]
	v_mfma_f32_16x16x32_bf16 v[102:105], v[134:137], v[198:201], v[102:105]
	v_mfma_f32_16x16x32_bf16 v[94:97], v[158:161], v[198:201], v[94:97]
	v_mfma_f32_16x16x32_bf16 v[86:89], v[134:137], v[206:209], v[86:89]
	v_mfma_f32_16x16x32_bf16 v[78:81], v[158:161], v[206:209], v[78:81]
	s_setprio 0
	s_setprio 1
	v_mfma_f32_16x16x32_bf16 v[114:117], v[162:165], v[178:181], v[114:117]
	v_mfma_f32_16x16x32_bf16 v[106:109], v[170:173], v[178:181], v[106:109]
	v_mfma_f32_16x16x32_bf16 v[98:101], v[162:165], v[186:189], v[98:101]
	v_mfma_f32_16x16x32_bf16 v[90:93], v[170:173], v[186:189], v[90:93]
	v_mfma_f32_16x16x32_bf16 v[82:85], v[162:165], v[194:197], v[82:85]
	v_mfma_f32_16x16x32_bf16 v[74:77], v[170:173], v[194:197], v[74:77]
	v_mfma_f32_16x16x32_bf16 v[70:73], v[162:165], v[202:205], v[70:73]
	v_mfma_f32_16x16x32_bf16 v[66:69], v[170:173], v[202:205], v[66:69]
	v_mfma_f32_16x16x32_bf16 v[114:117], v[166:169], v[182:185], v[114:117]
	v_mfma_f32_16x16x32_bf16 v[106:109], v[174:177], v[182:185], v[106:109]
	v_mfma_f32_16x16x32_bf16 v[98:101], v[166:169], v[190:193], v[98:101]
	v_mfma_f32_16x16x32_bf16 v[90:93], v[174:177], v[190:193], v[90:93]
	v_mfma_f32_16x16x32_bf16 v[82:85], v[166:169], v[198:201], v[82:85]
	v_mfma_f32_16x16x32_bf16 v[74:77], v[174:177], v[198:201], v[74:77]
	v_mfma_f32_16x16x32_bf16 v[70:73], v[166:169], v[206:209], v[70:73]
	v_mfma_f32_16x16x32_bf16 v[66:69], v[174:177], v[206:209], v[66:69]
	s_setprio 0
	s_barrier
	s_mov_b32 m0, s47
	ds_read_b128 v[178:181], v152 offset:16384
	ds_read_b128 v[182:185], v152 offset:17408
	ds_read_b128 v[186:189], v152 offset:18432
	ds_read_b128 v[190:193], v152 offset:19456
	ds_read_b128 v[194:197], v152 offset:20480
	ds_read_b128 v[198:201], v152 offset:21504
	ds_read_b128 v[202:205], v152 offset:22528
	ds_read_b128 v[206:209], v152 offset:23552
	s_nop 0
	global_load_lds_dwordx4 v145, s[26:27]
	s_mov_b32 m0, s48
	s_nop 0
	global_load_lds_dwordx4 v150, s[26:27]
	s_mov_b32 m0, s49
	s_nop 0
	global_load_lds_dwordx4 v145, s[34:35]
	s_mov_b32 m0, s50
	s_nop 0
	global_load_lds_dwordx4 v150, s[34:35]
	s_mov_b32 m0, s85
	s_nop 0
	global_load_lds_dwordx4 v141, s[24:25]
	s_mov_b32 m0, s38
	s_nop 0
	global_load_lds_dwordx4 v149, s[24:25]
	s_waitcnt vmcnt(8)
	s_waitcnt lgkmcnt(0)
	s_barrier
	s_setprio 1
	s_waitcnt lgkmcnt(0)
	v_mfma_f32_16x16x32_bf16 v[62:65], v[130:133], v[178:181], v[62:65]
	v_mfma_f32_16x16x32_bf16 v[58:61], v[154:157], v[178:181], v[58:61]
	v_mfma_f32_16x16x32_bf16 v[54:57], v[130:133], v[186:189], v[54:57]
	v_mfma_f32_16x16x32_bf16 v[46:49], v[154:157], v[186:189], v[46:49]
	v_mfma_f32_16x16x32_bf16 v[38:41], v[130:133], v[194:197], v[38:41]
	v_mfma_f32_16x16x32_bf16 v[30:33], v[154:157], v[194:197], v[30:33]
	v_mfma_f32_16x16x32_bf16 v[22:25], v[130:133], v[202:205], v[22:25]
	v_mfma_f32_16x16x32_bf16 v[14:17], v[154:157], v[202:205], v[14:17]
	v_mfma_f32_16x16x32_bf16 v[62:65], v[134:137], v[182:185], v[62:65]
	v_mfma_f32_16x16x32_bf16 v[58:61], v[158:161], v[182:185], v[58:61]
	v_mfma_f32_16x16x32_bf16 v[54:57], v[134:137], v[190:193], v[54:57]
	v_mfma_f32_16x16x32_bf16 v[46:49], v[158:161], v[190:193], v[46:49]
	v_mfma_f32_16x16x32_bf16 v[38:41], v[134:137], v[198:201], v[38:41]
	v_mfma_f32_16x16x32_bf16 v[30:33], v[158:161], v[198:201], v[30:33]
	v_mfma_f32_16x16x32_bf16 v[22:25], v[134:137], v[206:209], v[22:25]
	v_mfma_f32_16x16x32_bf16 v[14:17], v[158:161], v[206:209], v[14:17]
	s_setprio 0
	s_setprio 1
	v_mfma_f32_16x16x32_bf16 v[50:53], v[162:165], v[178:181], v[50:53]
	v_mfma_f32_16x16x32_bf16 v[42:45], v[170:173], v[178:181], v[42:45]
	v_mfma_f32_16x16x32_bf16 v[34:37], v[162:165], v[186:189], v[34:37]
	v_mfma_f32_16x16x32_bf16 v[26:29], v[170:173], v[186:189], v[26:29]
	v_mfma_f32_16x16x32_bf16 v[18:21], v[162:165], v[194:197], v[18:21]
	v_mfma_f32_16x16x32_bf16 v[10:13], v[170:173], v[194:197], v[10:13]
	v_mfma_f32_16x16x32_bf16 v[6:9], v[162:165], v[202:205], v[6:9]
	v_mfma_f32_16x16x32_bf16 v[2:5], v[170:173], v[202:205], v[2:5]
	v_mfma_f32_16x16x32_bf16 v[50:53], v[166:169], v[182:185], v[50:53]
	v_mfma_f32_16x16x32_bf16 v[42:45], v[174:177], v[182:185], v[42:45]
	v_mfma_f32_16x16x32_bf16 v[34:37], v[166:169], v[190:193], v[34:37]
	v_mfma_f32_16x16x32_bf16 v[26:29], v[174:177], v[190:193], v[26:29]
	v_mfma_f32_16x16x32_bf16 v[18:21], v[166:169], v[198:201], v[18:21]
	v_mfma_f32_16x16x32_bf16 v[10:13], v[174:177], v[198:201], v[10:13]
	v_mfma_f32_16x16x32_bf16 v[6:9], v[166:169], v[206:209], v[6:9]
	v_mfma_f32_16x16x32_bf16 v[2:5], v[174:177], v[206:209], v[2:5]
	s_setprio 0
	s_barrier
	v_add_u32_e32 v0, s51, v151
	ds_read_b128 v[130:133], v0
	ds_read_b128 v[134:137], v0 offset:1024
	ds_read_b128 v[154:157], v0 offset:2048
	ds_read_b128 v[158:161], v0 offset:3072
	v_add_u32_e32 v0, s52, v151
	ds_read_b128 v[162:165], v0
	ds_read_b128 v[166:169], v0 offset:1024
	ds_read_b128 v[170:173], v0 offset:2048
	ds_read_b128 v[174:177], v0 offset:3072
	s_mov_b32 m0, s39
	ds_read_b128 v[178:181], v152 offset:32768
	ds_read_b128 v[182:185], v152 offset:33792
	ds_read_b128 v[186:189], v152 offset:34816
	ds_read_b128 v[190:193], v152 offset:35840
	ds_read_b128 v[194:197], v152 offset:36864
	ds_read_b128 v[198:201], v152 offset:37888
	ds_read_b128 v[202:205], v152 offset:38912
	ds_read_b128 v[206:209], v152 offset:39936
	s_nop 0
	global_load_lds_dwordx4 v141, s[30:31]
	s_mov_b32 m0, s40
	s_nop 0
	global_load_lds_dwordx4 v149, s[30:31]
	s_waitcnt vmcnt(8)
	s_waitcnt lgkmcnt(0)
	s_barrier
	s_setprio 1
	s_waitcnt lgkmcnt(0)
	v_mfma_f32_16x16x32_bf16 v[126:129], v[130:133], v[178:181], v[126:129]
	v_mfma_f32_16x16x32_bf16 v[122:125], v[154:157], v[178:181], v[122:125]
	v_mfma_f32_16x16x32_bf16 v[118:121], v[130:133], v[186:189], v[118:121]
	v_mfma_f32_16x16x32_bf16 v[110:113], v[154:157], v[186:189], v[110:113]
	v_mfma_f32_16x16x32_bf16 v[102:105], v[130:133], v[194:197], v[102:105]
	v_mfma_f32_16x16x32_bf16 v[94:97], v[154:157], v[194:197], v[94:97]
	v_mfma_f32_16x16x32_bf16 v[86:89], v[130:133], v[202:205], v[86:89]
	v_mfma_f32_16x16x32_bf16 v[78:81], v[154:157], v[202:205], v[78:81]
	v_mfma_f32_16x16x32_bf16 v[126:129], v[134:137], v[182:185], v[126:129]
	v_mfma_f32_16x16x32_bf16 v[122:125], v[158:161], v[182:185], v[122:125]
	v_mfma_f32_16x16x32_bf16 v[118:121], v[134:137], v[190:193], v[118:121]
	v_mfma_f32_16x16x32_bf16 v[110:113], v[158:161], v[190:193], v[110:113]
	v_mfma_f32_16x16x32_bf16 v[102:105], v[134:137], v[198:201], v[102:105]
	v_mfma_f32_16x16x32_bf16 v[94:97], v[158:161], v[198:201], v[94:97]
	v_mfma_f32_16x16x32_bf16 v[86:89], v[134:137], v[206:209], v[86:89]
	v_mfma_f32_16x16x32_bf16 v[78:81], v[158:161], v[206:209], v[78:81]
	s_setprio 0
	s_setprio 1
	v_mfma_f32_16x16x32_bf16 v[114:117], v[162:165], v[178:181], v[114:117]
	v_mfma_f32_16x16x32_bf16 v[106:109], v[170:173], v[178:181], v[106:109]
	v_mfma_f32_16x16x32_bf16 v[98:101], v[162:165], v[186:189], v[98:101]
	v_mfma_f32_16x16x32_bf16 v[90:93], v[170:173], v[186:189], v[90:93]
	v_mfma_f32_16x16x32_bf16 v[82:85], v[162:165], v[194:197], v[82:85]
	v_mfma_f32_16x16x32_bf16 v[74:77], v[170:173], v[194:197], v[74:77]
	v_mfma_f32_16x16x32_bf16 v[70:73], v[162:165], v[202:205], v[70:73]
	v_mfma_f32_16x16x32_bf16 v[66:69], v[170:173], v[202:205], v[66:69]
	v_mfma_f32_16x16x32_bf16 v[114:117], v[166:169], v[182:185], v[114:117]
	v_mfma_f32_16x16x32_bf16 v[106:109], v[174:177], v[182:185], v[106:109]
	v_mfma_f32_16x16x32_bf16 v[98:101], v[166:169], v[190:193], v[98:101]
	v_mfma_f32_16x16x32_bf16 v[90:93], v[174:177], v[190:193], v[90:93]
	v_mfma_f32_16x16x32_bf16 v[82:85], v[166:169], v[198:201], v[82:85]
	v_mfma_f32_16x16x32_bf16 v[74:77], v[174:177], v[198:201], v[74:77]
	v_mfma_f32_16x16x32_bf16 v[70:73], v[166:169], v[206:209], v[70:73]
	v_mfma_f32_16x16x32_bf16 v[66:69], v[174:177], v[206:209], v[66:69]
	s_setprio 0
	s_barrier
	v_mov_b32_e32 v0, v145
	ds_read_b128 v[178:181], v152 offset:49152
	ds_read_b128 v[182:185], v152 offset:50176
	ds_read_b128 v[186:189], v152 offset:51200
	ds_read_b128 v[190:193], v152 offset:52224
	ds_read_b128 v[194:197], v152 offset:53248
	ds_read_b128 v[198:201], v152 offset:54272
	ds_read_b128 v[202:205], v152 offset:55296
	ds_read_b128 v[206:209], v152 offset:56320
	s_mov_b32 m0, s53
	v_lshl_add_u64 v[138:139], s[26:27], 0, v[0:1]
	v_lshl_add_u64 v[138:139], v[138:139], 0, s[90:91]
	v_mov_b32_e32 v0, v150
	global_load_lds_dwordx4 v[138:139], off
	s_mov_b32 m0, s54
	v_lshl_add_u64 v[138:139], s[26:27], 0, v[0:1]
	v_lshl_add_u64 v[138:139], v[138:139], 0, s[90:91]
	global_load_lds_dwordx4 v[138:139], off
	s_mov_b32 m0, s55
	s_nop 0
	global_load_lds_dwordx4 v145, s[28:29]
	s_mov_b32 m0, s56
	s_nop 0
	global_load_lds_dwordx4 v150, s[28:29]
	v_mov_b32_e32 v0, v141
	s_mov_b32 m0, s41
	v_lshl_add_u64 v[138:139], s[24:25], 0, v[0:1]
	v_lshl_add_u64 v[138:139], v[138:139], 0, s[90:91]
	v_mov_b32_e32 v0, v149
	global_load_lds_dwordx4 v[138:139], off
	s_mov_b32 m0, s42
	v_lshl_add_u64 v[138:139], s[24:25], 0, v[0:1]
	v_lshl_add_u64 v[138:139], v[138:139], 0, s[90:91]
	global_load_lds_dwordx4 v[138:139], off
	s_waitcnt vmcnt(8)
	s_waitcnt lgkmcnt(0)
	s_barrier
	s_setprio 1
	s_waitcnt lgkmcnt(0)
	v_mfma_f32_16x16x32_bf16 v[62:65], v[130:133], v[178:181], v[62:65]
	v_mfma_f32_16x16x32_bf16 v[58:61], v[154:157], v[178:181], v[58:61]
	v_mfma_f32_16x16x32_bf16 v[54:57], v[130:133], v[186:189], v[54:57]
	v_mfma_f32_16x16x32_bf16 v[46:49], v[154:157], v[186:189], v[46:49]
	v_mfma_f32_16x16x32_bf16 v[38:41], v[130:133], v[194:197], v[38:41]
	v_mfma_f32_16x16x32_bf16 v[30:33], v[154:157], v[194:197], v[30:33]
	v_mfma_f32_16x16x32_bf16 v[22:25], v[130:133], v[202:205], v[22:25]
	v_mfma_f32_16x16x32_bf16 v[14:17], v[154:157], v[202:205], v[14:17]
	v_mfma_f32_16x16x32_bf16 v[62:65], v[134:137], v[182:185], v[62:65]
	v_mfma_f32_16x16x32_bf16 v[58:61], v[158:161], v[182:185], v[58:61]
	v_mfma_f32_16x16x32_bf16 v[54:57], v[134:137], v[190:193], v[54:57]
	v_mfma_f32_16x16x32_bf16 v[46:49], v[158:161], v[190:193], v[46:49]
	v_mfma_f32_16x16x32_bf16 v[38:41], v[134:137], v[198:201], v[38:41]
	v_mfma_f32_16x16x32_bf16 v[30:33], v[158:161], v[198:201], v[30:33]
	v_mfma_f32_16x16x32_bf16 v[22:25], v[134:137], v[206:209], v[22:25]
	v_mfma_f32_16x16x32_bf16 v[14:17], v[158:161], v[206:209], v[14:17]
	s_setprio 0
	s_setprio 1
	v_mfma_f32_16x16x32_bf16 v[50:53], v[162:165], v[178:181], v[50:53]
	v_mfma_f32_16x16x32_bf16 v[42:45], v[170:173], v[178:181], v[42:45]
	v_mfma_f32_16x16x32_bf16 v[34:37], v[162:165], v[186:189], v[34:37]
	v_mfma_f32_16x16x32_bf16 v[26:29], v[170:173], v[186:189], v[26:29]
	v_mfma_f32_16x16x32_bf16 v[18:21], v[162:165], v[194:197], v[18:21]
	v_mfma_f32_16x16x32_bf16 v[10:13], v[170:173], v[194:197], v[10:13]
	v_mfma_f32_16x16x32_bf16 v[6:9], v[162:165], v[202:205], v[6:9]
	v_mfma_f32_16x16x32_bf16 v[2:5], v[170:173], v[202:205], v[2:5]
	v_mfma_f32_16x16x32_bf16 v[50:53], v[166:169], v[182:185], v[50:53]
	v_mfma_f32_16x16x32_bf16 v[42:45], v[174:177], v[182:185], v[42:45]
	v_mfma_f32_16x16x32_bf16 v[34:37], v[166:169], v[190:193], v[34:37]
	v_mfma_f32_16x16x32_bf16 v[26:29], v[174:177], v[190:193], v[26:29]
	v_mfma_f32_16x16x32_bf16 v[18:21], v[166:169], v[198:201], v[18:21]
	v_mfma_f32_16x16x32_bf16 v[10:13], v[174:177], v[198:201], v[10:13]
	v_mfma_f32_16x16x32_bf16 v[6:9], v[166:169], v[206:209], v[6:9]
	v_mfma_f32_16x16x32_bf16 v[2:5], v[174:177], v[206:209], v[2:5]
	s_setprio 0
	s_barrier
	s_mov_b64 s[26:27], -1
	s_andn2_b64 vcc, exec, s[22:23]
	s_mov_b64 s[22:23], 0
	s_mov_b64 s[28:29], 0x100
	s_cbranch_vccz .LBB0_918
	v_readlane_b32 s14, v254, 19
	v_readlane_b32 s15, v254, 20
	s_and_b64 vcc, exec, s[14:15]
	s_cbranch_vccz .LBB0_921
	s_barrier

.LBB0_1200:
	s_add_u32 s30, s24, s12
	s_addc_u32 s31, s25, s13
	s_add_u32 s14, s30, 0x1f000100
	s_addc_u32 s15, s31, 0
	s_add_u32 s16, s26, s12
	s_addc_u32 s17, s27, s13
	s_add_i32 s29, 0, 0x10000
	s_cmpk_eq_i32 s12, 0x700
	s_cselect_b32 s15, s11, s15
	s_cselect_b32 s14, s10, s14
	v_add_u32_e32 v0, s29, v134
	s_cselect_b32 s17, s5, s17
	s_cselect_b32 s16, s4, s16
	s_add_i32 s34, 0, 0x14000
	ds_read_b128 v[136:139], v0
	ds_read_b128 v[140:143], v0 offset:1024
	ds_read_b128 v[144:147], v0 offset:2048
	ds_read_b128 v[148:151], v0 offset:3072
	v_add_u32_e32 v0, s34, v134
	ds_read_b128 v[152:155], v0
	ds_read_b128 v[156:159], v0 offset:1024
	ds_read_b128 v[160:163], v0 offset:2048
	ds_read_b128 v[164:167], v0 offset:3072
	v_mov_b32_e32 v0, v130
	ds_read_b128 v[168:171], v135
	ds_read_b128 v[172:175], v135 offset:1024
	ds_read_b128 v[176:179], v135 offset:2048
	ds_read_b128 v[180:183], v135 offset:3072
	ds_read_b128 v[184:187], v135 offset:4096
	ds_read_b128 v[188:191], v135 offset:5120
	ds_read_b128 v[192:195], v135 offset:6144
	ds_read_b128 v[196:199], v135 offset:7168
	s_add_i32 m0, s85, 0xc000
	v_lshl_add_u64 v[200:201], s[30:31], 0, v[0:1]
	v_lshl_add_u64 v[200:201], v[200:201], 0, s[64:65]
	v_mov_b32_e32 v0, v132
	global_load_lds_dwordx4 v[200:201], off
	s_add_i32 m0, s85, 0xe000
	v_lshl_add_u64 v[200:201], s[30:31], 0, v[0:1]
	v_lshl_add_u64 v[200:201], v[200:201], 0, s[64:65]
	global_load_lds_dwordx4 v[200:201], off
	s_waitcnt vmcnt(8)
	s_waitcnt lgkmcnt(0)
	s_barrier
	s_setprio 1
	s_waitcnt lgkmcnt(0)
	v_mfma_f32_16x16x32_bf16 v[126:129], v[136:139], v[168:171], v[126:129]
	v_mfma_f32_16x16x32_bf16 v[122:125], v[144:147], v[168:171], v[122:125]
	v_mfma_f32_16x16x32_bf16 v[118:121], v[136:139], v[176:179], v[118:121]
	v_mfma_f32_16x16x32_bf16 v[114:117], v[144:147], v[176:179], v[114:117]
	v_mfma_f32_16x16x32_bf16 v[110:113], v[136:139], v[184:187], v[110:113]
	v_mfma_f32_16x16x32_bf16 v[106:109], v[144:147], v[184:187], v[106:109]
	v_mfma_f32_16x16x32_bf16 v[102:105], v[136:139], v[192:195], v[102:105]
	v_mfma_f32_16x16x32_bf16 v[98:101], v[144:147], v[192:195], v[98:101]
	v_mfma_f32_16x16x32_bf16 v[126:129], v[140:143], v[172:175], v[126:129]
	v_mfma_f32_16x16x32_bf16 v[122:125], v[148:151], v[172:175], v[122:125]
	v_mfma_f32_16x16x32_bf16 v[118:121], v[140:143], v[180:183], v[118:121]
	v_mfma_f32_16x16x32_bf16 v[114:117], v[148:151], v[180:183], v[114:117]
	v_mfma_f32_16x16x32_bf16 v[110:113], v[140:143], v[188:191], v[110:113]
	v_mfma_f32_16x16x32_bf16 v[106:109], v[148:151], v[188:191], v[106:109]
	v_mfma_f32_16x16x32_bf16 v[102:105], v[140:143], v[196:199], v[102:105]
	v_mfma_f32_16x16x32_bf16 v[98:101], v[148:151], v[196:199], v[98:101]
	s_setprio 0
	s_setprio 1
	v_mfma_f32_16x16x32_bf16 v[62:65], v[152:155], v[168:171], v[62:65]
	v_mfma_f32_16x16x32_bf16 v[58:61], v[160:163], v[168:171], v[58:61]
	v_mfma_f32_16x16x32_bf16 v[54:57], v[152:155], v[176:179], v[54:57]
	v_mfma_f32_16x16x32_bf16 v[50:53], v[160:163], v[176:179], v[50:53]
	v_mfma_f32_16x16x32_bf16 v[46:49], v[152:155], v[184:187], v[46:49]
	v_mfma_f32_16x16x32_bf16 v[42:45], v[160:163], v[184:187], v[42:45]
	v_mfma_f32_16x16x32_bf16 v[38:41], v[152:155], v[192:195], v[38:41]
	v_mfma_f32_16x16x32_bf16 v[34:37], v[160:163], v[192:195], v[34:37]
	v_mfma_f32_16x16x32_bf16 v[62:65], v[156:159], v[172:175], v[62:65]
	v_mfma_f32_16x16x32_bf16 v[58:61], v[164:167], v[172:175], v[58:61]
	v_mfma_f32_16x16x32_bf16 v[54:57], v[156:159], v[180:183], v[54:57]
	v_mfma_f32_16x16x32_bf16 v[50:53], v[164:167], v[180:183], v[50:53]
	v_mfma_f32_16x16x32_bf16 v[46:49], v[156:159], v[188:191], v[46:49]
	v_mfma_f32_16x16x32_bf16 v[42:45], v[164:167], v[188:191], v[42:45]
	v_mfma_f32_16x16x32_bf16 v[38:41], v[156:159], v[196:199], v[38:41]
	v_mfma_f32_16x16x32_bf16 v[34:37], v[164:167], v[196:199], v[34:37]
	s_setprio 0
	s_barrier
	s_add_i32 s29, s29, s33
	ds_read_b128 v[168:171], v135 offset:16384
	ds_read_b128 v[172:175], v135 offset:17408
	ds_read_b128 v[176:179], v135 offset:18432
	ds_read_b128 v[180:183], v135 offset:19456
	ds_read_b128 v[184:187], v135 offset:20480
	ds_read_b128 v[188:191], v135 offset:21504
	ds_read_b128 v[192:195], v135 offset:22528
	ds_read_b128 v[196:199], v135 offset:23552
	s_mov_b32 m0, s29
	s_nop 0
	global_load_lds_dwordx4 v131, s[16:17]
	s_add_i32 m0, s29, 0x2000
	s_add_u32 s30, s16, 0x40000
	global_load_lds_dwordx4 v133, s[16:17]
	s_addc_u32 s31, s17, 0
	s_add_i32 s29, s34, s33
	s_mov_b32 m0, s29
	s_nop 0
	global_load_lds_dwordx4 v131, s[30:31]
	s_add_i32 m0, s29, 0x2000
	s_nop 0
	global_load_lds_dwordx4 v133, s[30:31]
	s_waitcnt vmcnt(6)
	s_waitcnt lgkmcnt(0)
	s_barrier
	s_setprio 1
	s_waitcnt lgkmcnt(0)
	v_mfma_f32_16x16x32_bf16 v[94:97], v[136:139], v[168:171], v[94:97]
	v_mfma_f32_16x16x32_bf16 v[90:93], v[144:147], v[168:171], v[90:93]
	v_mfma_f32_16x16x32_bf16 v[86:89], v[136:139], v[176:179], v[86:89]
	v_mfma_f32_16x16x32_bf16 v[82:85], v[144:147], v[176:179], v[82:85]
	v_mfma_f32_16x16x32_bf16 v[78:81], v[136:139], v[184:187], v[78:81]
	v_mfma_f32_16x16x32_bf16 v[74:77], v[144:147], v[184:187], v[74:77]
	v_mfma_f32_16x16x32_bf16 v[70:73], v[136:139], v[192:195], v[70:73]
	v_mfma_f32_16x16x32_bf16 v[66:69], v[144:147], v[192:195], v[66:69]
	v_mfma_f32_16x16x32_bf16 v[94:97], v[140:143], v[172:175], v[94:97]
	v_mfma_f32_16x16x32_bf16 v[90:93], v[148:151], v[172:175], v[90:93]
	v_mfma_f32_16x16x32_bf16 v[86:89], v[140:143], v[180:183], v[86:89]
	v_mfma_f32_16x16x32_bf16 v[82:85], v[148:151], v[180:183], v[82:85]
	v_mfma_f32_16x16x32_bf16 v[78:81], v[140:143], v[188:191], v[78:81]
	v_mfma_f32_16x16x32_bf16 v[74:77], v[148:151], v[188:191], v[74:77]
	v_mfma_f32_16x16x32_bf16 v[70:73], v[140:143], v[196:199], v[70:73]
	v_mfma_f32_16x16x32_bf16 v[66:69], v[148:151], v[196:199], v[66:69]
	s_setprio 0
	s_setprio 1
	v_mfma_f32_16x16x32_bf16 v[30:33], v[152:155], v[168:171], v[30:33]
	v_mfma_f32_16x16x32_bf16 v[26:29], v[160:163], v[168:171], v[26:29]
	v_mfma_f32_16x16x32_bf16 v[22:25], v[152:155], v[176:179], v[22:25]
	v_mfma_f32_16x16x32_bf16 v[18:21], v[160:163], v[176:179], v[18:21]
	v_mfma_f32_16x16x32_bf16 v[14:17], v[152:155], v[184:187], v[14:17]
	v_mfma_f32_16x16x32_bf16 v[10:13], v[160:163], v[184:187], v[10:13]
	v_mfma_f32_16x16x32_bf16 v[6:9], v[152:155], v[192:195], v[6:9]
	v_mfma_f32_16x16x32_bf16 v[2:5], v[160:163], v[192:195], v[2:5]
	v_mfma_f32_16x16x32_bf16 v[30:33], v[156:159], v[172:175], v[30:33]
	v_mfma_f32_16x16x32_bf16 v[26:29], v[164:167], v[172:175], v[26:29]
	v_mfma_f32_16x16x32_bf16 v[22:25], v[156:159], v[180:183], v[22:25]
	v_mfma_f32_16x16x32_bf16 v[18:21], v[164:167], v[180:183], v[18:21]
	v_mfma_f32_16x16x32_bf16 v[14:17], v[156:159], v[188:191], v[14:17]
	v_mfma_f32_16x16x32_bf16 v[10:13], v[164:167], v[188:191], v[10:13]
	v_mfma_f32_16x16x32_bf16 v[6:9], v[156:159], v[196:199], v[6:9]
	v_mfma_f32_16x16x32_bf16 v[2:5], v[164:167], v[196:199], v[2:5]
	s_setprio 0
	s_barrier
	s_add_i32 s29, 0, 0x18000
	v_add_u32_e32 v0, s29, v134
	s_add_i32 s34, 0, 0x1c000
	ds_read_b128 v[136:139], v0
	ds_read_b128 v[140:143], v0 offset:1024
	ds_read_b128 v[144:147], v0 offset:2048
	ds_read_b128 v[148:151], v0 offset:3072
	v_add_u32_e32 v0, s34, v134
	ds_read_b128 v[152:155], v0
	ds_read_b128 v[156:159], v0 offset:1024
	ds_read_b128 v[160:163], v0 offset:2048
	ds_read_b128 v[164:167], v0 offset:3072
	s_add_u32 s30, s14, 0x40000
	ds_read_b128 v[168:171], v135 offset:32768
	ds_read_b128 v[172:175], v135 offset:33792
	ds_read_b128 v[176:179], v135 offset:34816
	ds_read_b128 v[180:183], v135 offset:35840
	ds_read_b128 v[184:187], v135 offset:36864
	ds_read_b128 v[188:191], v135 offset:37888
	ds_read_b128 v[192:195], v135 offset:38912
	ds_read_b128 v[196:199], v135 offset:39936
	s_addc_u32 s31, s15, 0
	s_mov_b32 m0, s85
	s_nop 0
	global_load_lds_dwordx4 v130, s[14:15]
	s_mov_b32 m0, s9
	s_nop 0
	global_load_lds_dwordx4 v132, s[14:15]
	s_mov_b32 m0, s20
	s_nop 0
	global_load_lds_dwordx4 v130, s[30:31]
	s_mov_b32 m0, s21
	s_nop 0
	global_load_lds_dwordx4 v132, s[30:31]
	s_waitcnt vmcnt(8)
	s_waitcnt lgkmcnt(0)
	s_barrier
	s_setprio 1
	s_waitcnt lgkmcnt(0)
	v_mfma_f32_16x16x32_bf16 v[126:129], v[136:139], v[168:171], v[126:129]
	v_mfma_f32_16x16x32_bf16 v[122:125], v[144:147], v[168:171], v[122:125]
	v_mfma_f32_16x16x32_bf16 v[118:121], v[136:139], v[176:179], v[118:121]
	v_mfma_f32_16x16x32_bf16 v[114:117], v[144:147], v[176:179], v[114:117]
	v_mfma_f32_16x16x32_bf16 v[110:113], v[136:139], v[184:187], v[110:113]
	v_mfma_f32_16x16x32_bf16 v[106:109], v[144:147], v[184:187], v[106:109]
	v_mfma_f32_16x16x32_bf16 v[102:105], v[136:139], v[192:195], v[102:105]
	v_mfma_f32_16x16x32_bf16 v[98:101], v[144:147], v[192:195], v[98:101]
	v_mfma_f32_16x16x32_bf16 v[126:129], v[140:143], v[172:175], v[126:129]
	v_mfma_f32_16x16x32_bf16 v[122:125], v[148:151], v[172:175], v[122:125]
	v_mfma_f32_16x16x32_bf16 v[118:121], v[140:143], v[180:183], v[118:121]
	v_mfma_f32_16x16x32_bf16 v[114:117], v[148:151], v[180:183], v[114:117]
	v_mfma_f32_16x16x32_bf16 v[110:113], v[140:143], v[188:191], v[110:113]
	v_mfma_f32_16x16x32_bf16 v[106:109], v[148:151], v[188:191], v[106:109]
	v_mfma_f32_16x16x32_bf16 v[102:105], v[140:143], v[196:199], v[102:105]
	v_mfma_f32_16x16x32_bf16 v[98:101], v[148:151], v[196:199], v[98:101]
	s_setprio 0
	s_setprio 1
	v_mfma_f32_16x16x32_bf16 v[62:65], v[152:155], v[168:171], v[62:65]
	v_mfma_f32_16x16x32_bf16 v[58:61], v[160:163], v[168:171], v[58:61]
	v_mfma_f32_16x16x32_bf16 v[54:57], v[152:155], v[176:179], v[54:57]
	v_mfma_f32_16x16x32_bf16 v[50:53], v[160:163], v[176:179], v[50:53]
	v_mfma_f32_16x16x32_bf16 v[46:49], v[152:155], v[184:187], v[46:49]
	v_mfma_f32_16x16x32_bf16 v[42:45], v[160:163], v[184:187], v[42:45]
	v_mfma_f32_16x16x32_bf16 v[38:41], v[152:155], v[192:195], v[38:41]
	v_mfma_f32_16x16x32_bf16 v[34:37], v[160:163], v[192:195], v[34:37]
	v_mfma_f32_16x16x32_bf16 v[62:65], v[156:159], v[172:175], v[62:65]
	v_mfma_f32_16x16x32_bf16 v[58:61], v[164:167], v[172:175], v[58:61]
	v_mfma_f32_16x16x32_bf16 v[54:57], v[156:159], v[180:183], v[54:57]
	v_mfma_f32_16x16x32_bf16 v[50:53], v[164:167], v[180:183], v[50:53]
	v_mfma_f32_16x16x32_bf16 v[46:49], v[156:159], v[188:191], v[46:49]
	v_mfma_f32_16x16x32_bf16 v[42:45], v[164:167], v[188:191], v[42:45]
	v_mfma_f32_16x16x32_bf16 v[38:41], v[156:159], v[196:199], v[38:41]
	v_mfma_f32_16x16x32_bf16 v[34:37], v[164:167], v[196:199], v[34:37]
	s_setprio 0
	s_barrier
	v_mov_b32_e32 v0, v131
	ds_read_b128 v[168:171], v135 offset:49152
	ds_read_b128 v[172:175], v135 offset:50176
	ds_read_b128 v[176:179], v135 offset:51200
	ds_read_b128 v[180:183], v135 offset:52224
	ds_read_b128 v[184:187], v135 offset:53248
	ds_read_b128 v[188:191], v135 offset:54272
	ds_read_b128 v[192:195], v135 offset:55296
	ds_read_b128 v[196:199], v135 offset:56320
	s_add_i32 s29, s29, s33
	v_lshl_add_u64 v[200:201], s[16:17], 0, v[0:1]
	v_lshl_add_u64 v[200:201], v[200:201], 0, s[90:91]
	s_mov_b32 m0, s29
	v_mov_b32_e32 v0, v133
	global_load_lds_dwordx4 v[200:201], off
	s_add_i32 m0, s29, 0x2000
	s_nop 0
	v_lshl_add_u64 v[200:201], s[16:17], 0, v[0:1]
	s_add_u32 s16, s16, 0x40080
	v_lshl_add_u64 v[200:201], v[200:201], 0, s[90:91]
	s_addc_u32 s17, s17, 0
	s_add_i32 s29, s34, s33
	global_load_lds_dwordx4 v[200:201], off
	s_mov_b32 m0, s29
	s_nop 0
	global_load_lds_dwordx4 v131, s[16:17]
	s_add_i32 m0, s29, 0x2000
	s_nop 0
	global_load_lds_dwordx4 v133, s[16:17]
	s_waitcnt vmcnt(6)
	s_waitcnt lgkmcnt(0)
	s_barrier
	s_setprio 1
	s_waitcnt lgkmcnt(0)
	v_mfma_f32_16x16x32_bf16 v[94:97], v[136:139], v[168:171], v[94:97]
	v_mfma_f32_16x16x32_bf16 v[90:93], v[144:147], v[168:171], v[90:93]
	v_mfma_f32_16x16x32_bf16 v[86:89], v[136:139], v[176:179], v[86:89]
	v_mfma_f32_16x16x32_bf16 v[82:85], v[144:147], v[176:179], v[82:85]
	v_mfma_f32_16x16x32_bf16 v[78:81], v[136:139], v[184:187], v[78:81]
	v_mfma_f32_16x16x32_bf16 v[74:77], v[144:147], v[184:187], v[74:77]
	v_mfma_f32_16x16x32_bf16 v[70:73], v[136:139], v[192:195], v[70:73]
	v_mfma_f32_16x16x32_bf16 v[66:69], v[144:147], v[192:195], v[66:69]
	v_mfma_f32_16x16x32_bf16 v[94:97], v[140:143], v[172:175], v[94:97]
	v_mfma_f32_16x16x32_bf16 v[90:93], v[148:151], v[172:175], v[90:93]
	v_mfma_f32_16x16x32_bf16 v[86:89], v[140:143], v[180:183], v[86:89]
	v_mfma_f32_16x16x32_bf16 v[82:85], v[148:151], v[180:183], v[82:85]
	v_mfma_f32_16x16x32_bf16 v[78:81], v[140:143], v[188:191], v[78:81]
	v_mfma_f32_16x16x32_bf16 v[74:77], v[148:151], v[188:191], v[74:77]
	v_mfma_f32_16x16x32_bf16 v[70:73], v[140:143], v[196:199], v[70:73]
	v_mfma_f32_16x16x32_bf16 v[66:69], v[148:151], v[196:199], v[66:69]
	s_setprio 0
	s_setprio 1
	v_mfma_f32_16x16x32_bf16 v[30:33], v[152:155], v[168:171], v[30:33]
	v_mfma_f32_16x16x32_bf16 v[26:29], v[160:163], v[168:171], v[26:29]
	v_mfma_f32_16x16x32_bf16 v[22:25], v[152:155], v[176:179], v[22:25]
	v_mfma_f32_16x16x32_bf16 v[18:21], v[160:163], v[176:179], v[18:21]
	v_mfma_f32_16x16x32_bf16 v[14:17], v[152:155], v[184:187], v[14:17]
	v_mfma_f32_16x16x32_bf16 v[10:13], v[160:163], v[184:187], v[10:13]
	v_mfma_f32_16x16x32_bf16 v[6:9], v[152:155], v[192:195], v[6:9]
	v_mfma_f32_16x16x32_bf16 v[2:5], v[160:163], v[192:195], v[2:5]
	v_mfma_f32_16x16x32_bf16 v[30:33], v[156:159], v[172:175], v[30:33]
	v_mfma_f32_16x16x32_bf16 v[26:29], v[164:167], v[172:175], v[26:29]
	v_mfma_f32_16x16x32_bf16 v[22:25], v[156:159], v[180:183], v[22:25]
	v_mfma_f32_16x16x32_bf16 v[18:21], v[164:167], v[180:183], v[18:21]
	v_mfma_f32_16x16x32_bf16 v[14:17], v[156:159], v[188:191], v[14:17]
	v_mfma_f32_16x16x32_bf16 v[10:13], v[164:167], v[188:191], v[10:13]
	v_mfma_f32_16x16x32_bf16 v[6:9], v[156:159], v[196:199], v[6:9]
	v_mfma_f32_16x16x32_bf16 v[2:5], v[164:167], v[196:199], v[2:5]
	s_setprio 0
	s_barrier
	v_mov_b32_e32 v0, v130
	s_mov_b32 m0, s22
	v_lshl_add_u64 v[198:199], s[14:15], 0, v[0:1]
	v_lshl_add_u64 v[198:199], v[198:199], 0, s[90:91]
	v_mov_b32_e32 v0, v132
	global_load_lds_dwordx4 v[198:199], off
	s_mov_b32 m0, s23
	v_lshl_add_u64 v[198:199], s[14:15], 0, v[0:1]
	v_lshl_add_u64 v[198:199], v[198:199], 0, s[90:91]
	global_load_lds_dwordx4 v[198:199], off
	s_add_i32 s28, s28, 2
	s_add_u32 s12, s12, 0x100
	s_addc_u32 s13, s13, 0
	s_cmp_gt_u32 s28, 13
	s_cbranch_scc0 .LBB0_1200
	s_add_u32 s4, s6, 0x2b400000
	s_addc_u32 s5, s7, 0
	s_mul_i32 s10, s94, 0x30000
	s_mul_hi_u32 s9, s94, 0x30000
	s_add_u32 s6, s6, s10
	s_addc_u32 s7, s7, s9
	s_lshl_b32 s8, s8, 8
	s_ashr_i32 s9, s18, 5
	s_add_i32 s8, s8, s87
	s_mul_hi_i32 s10, s9, 0x6000
	s_mulk_i32 s9, 0x6000
	s_add_u32 s6, s6, s9
	v_mbcnt_lo_u32_b32 v140, -1, 0
	v_mbcnt_hi_u32_b32 v140, -1, v140
	s_addc_u32 s7, s7, s10
	s_lshl_b32 s9, s19, 8
	v_lshrrev_b32_e32 v0, 1, v140
	v_and_or_b32 v0, v0, 24, s9
	v_or_b32_e32 v200, s72, v0
	v_lshlrev_b32_e32 v0, 2, v200
	v_lshl_add_u64 v[130:131], s[6:7], 0, v[0:1]
	s_mov_b64 s[6:7], 0x102000
	v_lshl_add_u64 v[138:139], v[130:131], 0, s[6:7]
	s_mov_b32 s6, 0x102000
	v_add_co_u32_e32 v130, vcc, s6, v130
	v_and_or_b32 v174, v140, 15, s8
	s_nop 0
	v_addc_co_u32_e32 v131, vcc, 0, v131, vcc
	global_load_dwordx4 v[130:133], v[130:131], off
	s_nop 0
	global_load_dwordx4 v[134:137], v[138:139], off offset:16
	s_cmp_lg_u64 s[2:3], 0
	v_or_b32_e32 v178, 16, v174
	v_or_b32_e32 v176, 32, v174
	v_or_b32_e32 v172, 48, v174
	v_add_u32_e32 v186, 0x80, v174
	v_add_u32_e32 v184, 0x90, v174
	v_add_u32_e32 v182, 0xa0, v174
	v_add_u32_e32 v180, 0xb0, v174
	s_cselect_b64 s[6:7], -1, 0
	s_cmp_eq_u64 s[2:3], 0
	v_ashrrev_i32_e32 v175, 31, v174
	v_ashrrev_i32_e32 v179, 31, v178
	v_ashrrev_i32_e32 v177, 31, v176
	v_ashrrev_i32_e32 v173, 31, v172
	v_lshlrev_b32_e32 v170, 1, v200
	v_ashrrev_i32_e32 v187, 31, v186
	v_ashrrev_i32_e32 v185, 31, v184
	v_ashrrev_i32_e32 v183, 31, v182
	v_ashrrev_i32_e32 v181, 31, v180
	s_waitcnt vmcnt(0)
	v_pk_add_f32 v[194:195], v[132:133], 1.0 op_sel_hi:[1,0]
	v_pk_add_f32 v[192:193], v[130:131], 1.0 op_sel_hi:[1,0]
	v_pk_add_f32 v[190:191], v[136:137], 1.0 op_sel_hi:[1,0]
	v_pk_add_f32 v[188:189], v[134:135], 1.0 op_sel_hi:[1,0]
	global_load_dwordx4 v[130:133], v[138:139], off offset:528
	global_load_dwordx4 v[134:137], v[138:139], off offset:512
	s_cbranch_scc1 .LBB0_1232
	v_lshlrev_b64 v[138:139], 12, v[174:175]
	v_lshl_add_u64 v[138:139], s[2:3], 0, v[138:139]
	v_lshl_add_u64 v[142:143], v[138:139], 0, v[0:1]
	global_load_dwordx4 v[138:141], v[142:143], off offset:16
	s_nop 0
	global_load_dwordx4 v[142:145], v[142:143], off
	v_lshlrev_b64 v[146:147], 12, v[178:179]
	v_lshl_add_u64 v[146:147], s[2:3], 0, v[146:147]
	v_lshl_add_u64 v[150:151], v[146:147], 0, v[0:1]
	global_load_dwordx4 v[146:149], v[150:151], off offset:16
	s_nop 0
	global_load_dwordx4 v[150:153], v[150:151], off
	v_lshlrev_b64 v[154:155], 12, v[176:177]
	v_lshl_add_u64 v[154:155], s[2:3], 0, v[154:155]
	v_lshl_add_u64 v[158:159], v[154:155], 0, v[0:1]
	global_load_dwordx4 v[154:157], v[158:159], off offset:16
	s_nop 0
	global_load_dwordx4 v[158:161], v[158:159], off
	v_lshlrev_b64 v[162:163], 12, v[172:173]
	v_lshl_add_u64 v[162:163], s[2:3], 0, v[162:163]
	v_lshl_add_u64 v[166:167], v[162:163], 0, v[0:1]
	global_load_dwordx4 v[162:165], v[166:167], off offset:16
	s_nop 0
	global_load_dwordx4 v[166:169], v[166:167], off
	v_lshlrev_b64 v[196:197], 11, v[174:175]
	v_lshl_add_u64 v[196:197], s[4:5], 0, v[196:197]
	v_mov_b32_e32 v171, v1
	v_lshl_add_u64 v[196:197], v[196:197], 0, v[170:171]
	s_waitcnt vmcnt(7)
	v_pk_fma_f32 v[198:199], v[124:125], v[190:191], v[140:141]
	s_waitcnt vmcnt(6)
	v_pk_fma_f32 v[144:145], v[128:129], v[194:195], v[144:145]
	v_pk_fma_f32 v[142:143], v[126:127], v[192:193], v[142:143]
	v_pk_fma_f32 v[140:141], v[122:123], v[188:189], v[138:139]
	v_cvt_pk_bf16_f32 v138, v142, v143
	v_cvt_pk_bf16_f32 v139, v144, v145
	v_cvt_pk_bf16_f32 v140, v140, v141
	v_cvt_pk_bf16_f32 v141, v198, v199
	global_store_dwordx4 v[196:197], v[138:141], off
	s_waitcnt vmcnt(6)
	v_pk_fma_f32 v[144:145], v[116:117], v[190:191], v[148:149]
	v_pk_fma_f32 v[146:147], v[114:115], v[188:189], v[146:147]
	v_lshlrev_b64 v[138:139], 11, v[178:179]
	v_lshl_add_u64 v[138:139], s[4:5], 0, v[138:139]
	v_lshl_add_u64 v[142:143], v[138:139], 0, v[170:171]
	s_waitcnt vmcnt(5)
	v_pk_fma_f32 v[140:141], v[120:121], v[194:195], v[152:153]
	v_pk_fma_f32 v[138:139], v[118:119], v[192:193], v[150:151]
	v_lshlrev_b64 v[196:197], 11, v[186:187]
	v_cvt_pk_bf16_f32 v138, v138, v139
	v_cvt_pk_bf16_f32 v139, v140, v141
	v_cvt_pk_bf16_f32 v140, v146, v147
	v_cvt_pk_bf16_f32 v141, v144, v145
	global_store_dwordx4 v[142:143], v[138:141], off
	s_waitcnt vmcnt(5)
	v_pk_fma_f32 v[144:145], v[108:109], v[190:191], v[156:157]
	v_pk_fma_f32 v[146:147], v[106:107], v[188:189], v[154:155]
	v_lshlrev_b64 v[138:139], 11, v[176:177]
	v_lshl_add_u64 v[138:139], s[4:5], 0, v[138:139]
	v_lshl_add_u64 v[142:143], v[138:139], 0, v[170:171]
	s_waitcnt vmcnt(4)
	v_pk_fma_f32 v[140:141], v[112:113], v[194:195], v[160:161]
	v_pk_fma_f32 v[138:139], v[110:111], v[192:193], v[158:159]
	v_lshl_add_u64 v[196:197], s[4:5], 0, v[196:197]
	v_cvt_pk_bf16_f32 v138, v138, v139
	v_cvt_pk_bf16_f32 v139, v140, v141
	v_cvt_pk_bf16_f32 v140, v146, v147
	v_cvt_pk_bf16_f32 v141, v144, v145
	global_store_dwordx4 v[142:143], v[138:141], off
	s_waitcnt vmcnt(4)
	v_pk_fma_f32 v[144:145], v[100:101], v[190:191], v[164:165]
	v_pk_fma_f32 v[146:147], v[98:99], v[188:189], v[162:163]
	v_lshlrev_b64 v[138:139], 11, v[172:173]
	v_lshl_add_u64 v[138:139], s[4:5], 0, v[138:139]
	v_lshl_add_u64 v[142:143], v[138:139], 0, v[170:171]
	s_waitcnt vmcnt(3)
	v_pk_fma_f32 v[140:141], v[104:105], v[194:195], v[168:169]
	v_pk_fma_f32 v[138:139], v[102:103], v[192:193], v[166:167]
	v_lshl_add_u64 v[196:197], v[196:197], 0, v[170:171]
	v_cvt_pk_bf16_f32 v138, v138, v139
	v_cvt_pk_bf16_f32 v139, v140, v141
	v_cvt_pk_bf16_f32 v140, v146, v147
	v_cvt_pk_bf16_f32 v141, v144, v145
	global_store_dwordx4 v[142:143], v[138:141], off
	v_lshlrev_b64 v[146:147], 12, v[182:183]
	v_lshl_add_u64 v[146:147], s[2:3], 0, v[146:147]
	v_lshlrev_b64 v[138:139], 12, v[186:187]
	v_lshl_add_u64 v[138:139], s[2:3], 0, v[138:139]
	v_lshl_add_u64 v[138:139], v[138:139], 0, v[0:1]
	global_load_dwordx4 v[154:157], v[138:139], off offset:16
	global_load_dwordx4 v[158:161], v[138:139], off
	v_lshlrev_b64 v[138:139], 12, v[184:185]
	v_lshl_add_u64 v[138:139], s[2:3], 0, v[138:139]
	v_lshl_add_u64 v[142:143], v[138:139], 0, v[0:1]
	global_load_dwordx4 v[138:141], v[142:143], off offset:16
	s_nop 0
	global_load_dwordx4 v[142:145], v[142:143], off
	v_lshl_add_u64 v[146:147], v[146:147], 0, v[0:1]
	global_load_dwordx4 v[162:165], v[146:147], off offset:16
	global_load_dwordx4 v[166:169], v[146:147], off
	v_lshlrev_b64 v[146:147], 12, v[180:181]
	v_lshl_add_u64 v[146:147], s[2:3], 0, v[146:147]
	v_lshl_add_u64 v[150:151], v[146:147], 0, v[0:1]
	global_load_dwordx4 v[146:149], v[150:151], off offset:16
	s_nop 0
	global_load_dwordx4 v[150:153], v[150:151], off
	s_waitcnt vmcnt(7)
	v_pk_fma_f32 v[198:199], v[92:93], v[190:191], v[156:157]
	s_waitcnt vmcnt(6)
	v_pk_fma_f32 v[160:161], v[96:97], v[194:195], v[160:161]
	v_pk_fma_f32 v[158:159], v[94:95], v[192:193], v[158:159]
	v_pk_fma_f32 v[156:157], v[90:91], v[188:189], v[154:155]
	v_cvt_pk_bf16_f32 v154, v158, v159
	v_cvt_pk_bf16_f32 v155, v160, v161
	v_cvt_pk_bf16_f32 v156, v156, v157
	v_cvt_pk_bf16_f32 v157, v198, v199
	global_store_dwordx4 v[196:197], v[154:157], off
	s_waitcnt vmcnt(5)
	v_pk_fma_f32 v[144:145], v[88:89], v[194:195], v[144:145]
	v_pk_fma_f32 v[142:143], v[86:87], v[192:193], v[142:143]
	v_lshlrev_b64 v[154:155], 11, v[184:185]
	v_lshl_add_u64 v[154:155], s[4:5], 0, v[154:155]
	v_pk_fma_f32 v[156:157], v[84:85], v[190:191], v[140:141]
	v_pk_fma_f32 v[140:141], v[82:83], v[188:189], v[138:139]
	v_lshl_add_u64 v[154:155], v[154:155], 0, v[170:171]
	v_cvt_pk_bf16_f32 v138, v142, v143
	v_cvt_pk_bf16_f32 v139, v144, v145
	v_cvt_pk_bf16_f32 v140, v140, v141
	v_cvt_pk_bf16_f32 v141, v156, v157
	global_store_dwordx4 v[154:155], v[138:141], off
	s_waitcnt vmcnt(5)
	v_pk_fma_f32 v[144:145], v[76:77], v[190:191], v[164:165]
	v_pk_fma_f32 v[154:155], v[74:75], v[188:189], v[162:163]
	v_lshlrev_b64 v[138:139], 11, v[182:183]
	v_lshl_add_u64 v[138:139], s[4:5], 0, v[138:139]
	v_lshl_add_u64 v[142:143], v[138:139], 0, v[170:171]
	s_waitcnt vmcnt(4)
	v_pk_fma_f32 v[140:141], v[80:81], v[194:195], v[168:169]
	v_pk_fma_f32 v[138:139], v[78:79], v[192:193], v[166:167]
	s_waitcnt vmcnt(3)
	v_pk_fma_f32 v[146:147], v[66:67], v[188:189], v[146:147]
	v_cvt_pk_bf16_f32 v138, v138, v139
	v_cvt_pk_bf16_f32 v139, v140, v141
	v_cvt_pk_bf16_f32 v140, v154, v155
	v_cvt_pk_bf16_f32 v141, v144, v145
	global_store_dwordx4 v[142:143], v[138:141], off
	v_pk_fma_f32 v[144:145], v[68:69], v[190:191], v[148:149]
	s_nop 0
	v_lshlrev_b64 v[138:139], 11, v[180:181]
	v_lshl_add_u64 v[138:139], s[4:5], 0, v[138:139]
	v_lshl_add_u64 v[142:143], v[138:139], 0, v[170:171]
	s_waitcnt vmcnt(3)
	v_pk_fma_f32 v[140:141], v[72:73], v[194:195], v[152:153]
	v_pk_fma_f32 v[138:139], v[70:71], v[192:193], v[150:151]
	s_nop 0
	v_cvt_pk_bf16_f32 v138, v138, v139
	v_cvt_pk_bf16_f32 v139, v140, v141
	v_cvt_pk_bf16_f32 v140, v146, v147
	v_cvt_pk_bf16_f32 v141, v144, v145
	global_store_dwordx4 v[142:143], v[138:141], off
	s_cbranch_execnz .LBB0_1204

.LBB0_1508:
	s_add_u32 s42, s40, 0xfffe0080
	s_addc_u32 s43, s41, -1
	s_add_i32 s68, 0, 0x10000
	s_cmp_eq_u32 s67, 4
	s_cselect_b32 s43, s23, s43
	s_cselect_b32 s42, s29, s42
	v_add_u32_e32 v0, s68, v157
	s_cselect_b32 s45, s31, s66
	s_cselect_b32 s44, s30, s37
	s_add_i32 s70, 0, 0x14000
	ds_read_b128 v[82:85], v0
	ds_read_b128 v[86:89], v0 offset:1024
	ds_read_b128 v[90:93], v0 offset:2048
	ds_read_b128 v[94:97], v0 offset:3072
	v_add_u32_e32 v0, s70, v157
	ds_read_b128 v[160:163], v0
	ds_read_b128 v[164:167], v0 offset:1024
	ds_read_b128 v[168:171], v0 offset:2048
	ds_read_b128 v[172:175], v0 offset:3072
	ds_read_b128 v[176:179], v159
	ds_read_b128 v[180:183], v159 offset:1024
	ds_read_b128 v[184:187], v159 offset:2048
	ds_read_b128 v[188:191], v159 offset:3072
	ds_read_b128 v[192:195], v159 offset:4096
	ds_read_b128 v[196:199], v159 offset:5120
	ds_read_b128 v[200:203], v159 offset:6144
	ds_read_b128 v[204:207], v159 offset:7168
	s_add_i32 m0, s85, 0xc000
	s_nop 0
	global_load_lds_dwordx4 v149, s[40:41]
	s_add_i32 m0, s85, 0xe000
	s_nop 0
	global_load_lds_dwordx4 v153, s[40:41]
	s_waitcnt vmcnt(8)
	s_waitcnt lgkmcnt(0)
	s_barrier
	s_setprio 1
	s_waitcnt lgkmcnt(0)
	v_mfma_i32_16x16x64_i8 v[142:145], v[82:85], v[176:179], v[142:145]
	v_mfma_i32_16x16x64_i8 v[134:137], v[90:93], v[176:179], v[134:137]
	v_mfma_i32_16x16x64_i8 v[126:129], v[82:85], v[184:187], v[126:129]
	v_mfma_i32_16x16x64_i8 v[122:125], v[90:93], v[184:187], v[122:125]
	v_mfma_i32_16x16x64_i8 v[110:113], v[82:85], v[192:195], v[110:113]
	v_mfma_i32_16x16x64_i8 v[106:109], v[90:93], v[192:195], v[106:109]
	v_mfma_i32_16x16x64_i8 v[78:81], v[82:85], v[200:203], v[78:81]
	v_mfma_i32_16x16x64_i8 v[74:77], v[90:93], v[200:203], v[74:77]
	v_mfma_i32_16x16x64_i8 v[142:145], v[86:89], v[180:183], v[142:145]
	v_mfma_i32_16x16x64_i8 v[134:137], v[94:97], v[180:183], v[134:137]
	v_mfma_i32_16x16x64_i8 v[126:129], v[86:89], v[188:191], v[126:129]
	v_mfma_i32_16x16x64_i8 v[122:125], v[94:97], v[188:191], v[122:125]
	v_mfma_i32_16x16x64_i8 v[110:113], v[86:89], v[196:199], v[110:113]
	v_mfma_i32_16x16x64_i8 v[106:109], v[94:97], v[196:199], v[106:109]
	v_mfma_i32_16x16x64_i8 v[78:81], v[86:89], v[204:207], v[78:81]
	v_mfma_i32_16x16x64_i8 v[74:77], v[94:97], v[204:207], v[74:77]
	s_setprio 0
	s_setprio 1
	v_mfma_i32_16x16x64_i8 v[138:141], v[160:163], v[176:179], v[138:141]
	v_mfma_i32_16x16x64_i8 v[130:133], v[168:171], v[176:179], v[130:133]
	v_mfma_i32_16x16x64_i8 v[118:121], v[160:163], v[184:187], v[118:121]
	v_mfma_i32_16x16x64_i8 v[114:117], v[168:171], v[184:187], v[114:117]
	v_mfma_i32_16x16x64_i8 v[102:105], v[160:163], v[192:195], v[102:105]
	v_mfma_i32_16x16x64_i8 v[98:101], v[168:171], v[192:195], v[98:101]
	v_mfma_i32_16x16x64_i8 v[70:73], v[160:163], v[200:203], v[70:73]
	v_mfma_i32_16x16x64_i8 v[66:69], v[168:171], v[200:203], v[66:69]
	v_mfma_i32_16x16x64_i8 v[138:141], v[164:167], v[180:183], v[138:141]
	v_mfma_i32_16x16x64_i8 v[130:133], v[172:175], v[180:183], v[130:133]
	v_mfma_i32_16x16x64_i8 v[118:121], v[164:167], v[188:191], v[118:121]
	v_mfma_i32_16x16x64_i8 v[114:117], v[172:175], v[188:191], v[114:117]
	v_mfma_i32_16x16x64_i8 v[102:105], v[164:167], v[196:199], v[102:105]
	v_mfma_i32_16x16x64_i8 v[98:101], v[172:175], v[196:199], v[98:101]
	v_mfma_i32_16x16x64_i8 v[70:73], v[164:167], v[204:207], v[70:73]
	v_mfma_i32_16x16x64_i8 v[66:69], v[172:175], v[204:207], v[66:69]
	s_setprio 0
	s_barrier
	s_add_i32 s68, s68, s33
	ds_read_b128 v[176:179], v159 offset:16384
	ds_read_b128 v[180:183], v159 offset:17408
	ds_read_b128 v[184:187], v159 offset:18432
	ds_read_b128 v[188:191], v159 offset:19456
	ds_read_b128 v[192:195], v159 offset:20480
	ds_read_b128 v[196:199], v159 offset:21504
	ds_read_b128 v[200:203], v159 offset:22528
	ds_read_b128 v[204:207], v159 offset:23552
	s_mov_b32 m0, s68
	s_nop 0
	global_load_lds_dwordx4 v151, s[44:45]
	s_add_i32 m0, s68, 0x2000
	s_add_u32 s68, s44, 0x20000
	global_load_lds_dwordx4 v155, s[44:45]
	s_addc_u32 s69, s45, 0
	s_add_i32 s70, s70, s33
	s_mov_b32 m0, s70
	s_nop 0
	global_load_lds_dwordx4 v151, s[68:69]
	s_add_i32 m0, s70, 0x2000
	s_nop 0
	global_load_lds_dwordx4 v155, s[68:69]
	s_waitcnt vmcnt(6)
	s_waitcnt lgkmcnt(0)
	s_barrier
	s_setprio 1
	s_waitcnt lgkmcnt(0)
	v_mfma_i32_16x16x64_i8 v[62:65], v[82:85], v[176:179], v[62:65]
	v_mfma_i32_16x16x64_i8 v[58:61], v[90:93], v[176:179], v[58:61]
	v_mfma_i32_16x16x64_i8 v[46:49], v[82:85], v[184:187], v[46:49]
	v_mfma_i32_16x16x64_i8 v[42:45], v[90:93], v[184:187], v[42:45]
	v_mfma_i32_16x16x64_i8 v[30:33], v[82:85], v[192:195], v[30:33]
	v_mfma_i32_16x16x64_i8 v[26:29], v[90:93], v[192:195], v[26:29]
	v_mfma_i32_16x16x64_i8 v[14:17], v[82:85], v[200:203], v[14:17]
	v_mfma_i32_16x16x64_i8 v[10:13], v[90:93], v[200:203], v[10:13]
	v_mfma_i32_16x16x64_i8 v[62:65], v[86:89], v[180:183], v[62:65]
	v_mfma_i32_16x16x64_i8 v[58:61], v[94:97], v[180:183], v[58:61]
	v_mfma_i32_16x16x64_i8 v[46:49], v[86:89], v[188:191], v[46:49]
	v_mfma_i32_16x16x64_i8 v[42:45], v[94:97], v[188:191], v[42:45]
	v_mfma_i32_16x16x64_i8 v[30:33], v[86:89], v[196:199], v[30:33]
	v_mfma_i32_16x16x64_i8 v[26:29], v[94:97], v[196:199], v[26:29]
	v_mfma_i32_16x16x64_i8 v[14:17], v[86:89], v[204:207], v[14:17]
	v_mfma_i32_16x16x64_i8 v[10:13], v[94:97], v[204:207], v[10:13]
	s_setprio 0
	s_setprio 1
	v_mfma_i32_16x16x64_i8 v[54:57], v[160:163], v[176:179], v[54:57]
	v_mfma_i32_16x16x64_i8 v[50:53], v[168:171], v[176:179], v[50:53]
	v_mfma_i32_16x16x64_i8 v[38:41], v[160:163], v[184:187], v[38:41]
	v_mfma_i32_16x16x64_i8 v[34:37], v[168:171], v[184:187], v[34:37]
	v_mfma_i32_16x16x64_i8 v[22:25], v[160:163], v[192:195], v[22:25]
	v_mfma_i32_16x16x64_i8 v[18:21], v[168:171], v[192:195], v[18:21]
	v_mfma_i32_16x16x64_i8 v[6:9], v[160:163], v[200:203], v[6:9]
	v_mfma_i32_16x16x64_i8 v[2:5], v[168:171], v[200:203], v[2:5]
	v_mfma_i32_16x16x64_i8 v[54:57], v[164:167], v[180:183], v[54:57]
	v_mfma_i32_16x16x64_i8 v[50:53], v[172:175], v[180:183], v[50:53]
	v_mfma_i32_16x16x64_i8 v[38:41], v[164:167], v[188:191], v[38:41]
	v_mfma_i32_16x16x64_i8 v[34:37], v[172:175], v[188:191], v[34:37]
	v_mfma_i32_16x16x64_i8 v[22:25], v[164:167], v[196:199], v[22:25]
	v_mfma_i32_16x16x64_i8 v[18:21], v[172:175], v[196:199], v[18:21]
	v_mfma_i32_16x16x64_i8 v[6:9], v[164:167], v[204:207], v[6:9]
	v_mfma_i32_16x16x64_i8 v[2:5], v[172:175], v[204:207], v[2:5]
	s_setprio 0
	s_barrier
	s_add_i32 s70, 0, 0x18000
	v_add_u32_e32 v0, s70, v157
	s_add_i32 s71, 0, 0x1c000
	ds_read_b128 v[82:85], v0
	ds_read_b128 v[86:89], v0 offset:1024
	ds_read_b128 v[90:93], v0 offset:2048
	ds_read_b128 v[94:97], v0 offset:3072
	v_add_u32_e32 v0, s71, v157
	ds_read_b128 v[160:163], v0
	ds_read_b128 v[164:167], v0 offset:1024
	ds_read_b128 v[168:171], v0 offset:2048
	ds_read_b128 v[172:175], v0 offset:3072
	s_add_u32 s68, s42, 0x20000
	ds_read_b128 v[176:179], v159 offset:32768
	ds_read_b128 v[180:183], v159 offset:33792
	ds_read_b128 v[184:187], v159 offset:34816
	ds_read_b128 v[188:191], v159 offset:35840
	ds_read_b128 v[192:195], v159 offset:36864
	ds_read_b128 v[196:199], v159 offset:37888
	ds_read_b128 v[200:203], v159 offset:38912
	ds_read_b128 v[204:207], v159 offset:39936
	s_addc_u32 s69, s43, 0
	s_mov_b32 m0, s85
	s_nop 0
	global_load_lds_dwordx4 v149, s[42:43]
	s_mov_b32 m0, s56
	s_nop 0
	global_load_lds_dwordx4 v153, s[42:43]
	s_mov_b32 m0, s57
	s_nop 0
	global_load_lds_dwordx4 v149, s[68:69]
	s_mov_b32 m0, s58
	s_nop 0
	global_load_lds_dwordx4 v153, s[68:69]
	s_waitcnt vmcnt(8)
	s_waitcnt lgkmcnt(0)
	s_barrier
	s_setprio 1
	s_waitcnt lgkmcnt(0)
	v_mfma_i32_16x16x64_i8 v[142:145], v[82:85], v[176:179], v[142:145]
	v_mfma_i32_16x16x64_i8 v[134:137], v[90:93], v[176:179], v[134:137]
	v_mfma_i32_16x16x64_i8 v[126:129], v[82:85], v[184:187], v[126:129]
	v_mfma_i32_16x16x64_i8 v[122:125], v[90:93], v[184:187], v[122:125]
	v_mfma_i32_16x16x64_i8 v[110:113], v[82:85], v[192:195], v[110:113]
	v_mfma_i32_16x16x64_i8 v[106:109], v[90:93], v[192:195], v[106:109]
	v_mfma_i32_16x16x64_i8 v[78:81], v[82:85], v[200:203], v[78:81]
	v_mfma_i32_16x16x64_i8 v[74:77], v[90:93], v[200:203], v[74:77]
	v_mfma_i32_16x16x64_i8 v[142:145], v[86:89], v[180:183], v[142:145]
	v_mfma_i32_16x16x64_i8 v[134:137], v[94:97], v[180:183], v[134:137]
	v_mfma_i32_16x16x64_i8 v[126:129], v[86:89], v[188:191], v[126:129]
	v_mfma_i32_16x16x64_i8 v[122:125], v[94:97], v[188:191], v[122:125]
	v_mfma_i32_16x16x64_i8 v[110:113], v[86:89], v[196:199], v[110:113]
	v_mfma_i32_16x16x64_i8 v[106:109], v[94:97], v[196:199], v[106:109]
	v_mfma_i32_16x16x64_i8 v[78:81], v[86:89], v[204:207], v[78:81]
	v_mfma_i32_16x16x64_i8 v[74:77], v[94:97], v[204:207], v[74:77]
	s_setprio 0
	s_setprio 1
	v_mfma_i32_16x16x64_i8 v[138:141], v[160:163], v[176:179], v[138:141]
	v_mfma_i32_16x16x64_i8 v[130:133], v[168:171], v[176:179], v[130:133]
	v_mfma_i32_16x16x64_i8 v[118:121], v[160:163], v[184:187], v[118:121]
	v_mfma_i32_16x16x64_i8 v[114:117], v[168:171], v[184:187], v[114:117]
	v_mfma_i32_16x16x64_i8 v[102:105], v[160:163], v[192:195], v[102:105]
	v_mfma_i32_16x16x64_i8 v[98:101], v[168:171], v[192:195], v[98:101]
	v_mfma_i32_16x16x64_i8 v[70:73], v[160:163], v[200:203], v[70:73]
	v_mfma_i32_16x16x64_i8 v[66:69], v[168:171], v[200:203], v[66:69]
	v_mfma_i32_16x16x64_i8 v[138:141], v[164:167], v[180:183], v[138:141]
	v_mfma_i32_16x16x64_i8 v[130:133], v[172:175], v[180:183], v[130:133]
	v_mfma_i32_16x16x64_i8 v[118:121], v[164:167], v[188:191], v[118:121]
	v_mfma_i32_16x16x64_i8 v[114:117], v[172:175], v[188:191], v[114:117]
	v_mfma_i32_16x16x64_i8 v[102:105], v[164:167], v[196:199], v[102:105]
	v_mfma_i32_16x16x64_i8 v[98:101], v[172:175], v[196:199], v[98:101]
	v_mfma_i32_16x16x64_i8 v[70:73], v[164:167], v[204:207], v[70:73]
	v_mfma_i32_16x16x64_i8 v[66:69], v[172:175], v[204:207], v[66:69]
	s_setprio 0
	s_barrier
	v_mov_b32_e32 v0, v151
	ds_read_b128 v[176:179], v159 offset:49152
	ds_read_b128 v[180:183], v159 offset:50176
	ds_read_b128 v[184:187], v159 offset:51200
	ds_read_b128 v[188:191], v159 offset:52224
	ds_read_b128 v[192:195], v159 offset:53248
	ds_read_b128 v[196:199], v159 offset:54272
	ds_read_b128 v[200:203], v159 offset:55296
	ds_read_b128 v[204:207], v159 offset:56320
	s_add_i32 s68, s70, s33
	v_lshl_add_u64 v[146:147], s[44:45], 0, v[0:1]
	v_lshl_add_u64 v[146:147], v[146:147], 0, s[90:91]
	s_mov_b32 m0, s68
	v_mov_b32_e32 v0, v155
	global_load_lds_dwordx4 v[146:147], off
	s_add_i32 m0, s68, 0x2000
	s_nop 0
	v_lshl_add_u64 v[146:147], s[44:45], 0, v[0:1]
	s_add_u32 s44, s44, 0x20080
	v_lshl_add_u64 v[146:147], v[146:147], 0, s[90:91]
	s_addc_u32 s45, s45, 0
	s_add_i32 s68, s71, s33
	global_load_lds_dwordx4 v[146:147], off
	s_mov_b32 m0, s68
	s_nop 0
	global_load_lds_dwordx4 v151, s[44:45]
	s_add_i32 m0, s68, 0x2000
	s_nop 0
	global_load_lds_dwordx4 v155, s[44:45]
	s_waitcnt vmcnt(6)
	s_waitcnt lgkmcnt(0)
	s_barrier
	s_setprio 1
	s_waitcnt lgkmcnt(0)
	v_mfma_i32_16x16x64_i8 v[62:65], v[82:85], v[176:179], v[62:65]
	v_mfma_i32_16x16x64_i8 v[58:61], v[90:93], v[176:179], v[58:61]
	v_mfma_i32_16x16x64_i8 v[46:49], v[82:85], v[184:187], v[46:49]
	v_mfma_i32_16x16x64_i8 v[42:45], v[90:93], v[184:187], v[42:45]
	v_mfma_i32_16x16x64_i8 v[30:33], v[82:85], v[192:195], v[30:33]
	v_mfma_i32_16x16x64_i8 v[26:29], v[90:93], v[192:195], v[26:29]
	v_mfma_i32_16x16x64_i8 v[14:17], v[82:85], v[200:203], v[14:17]
	v_mfma_i32_16x16x64_i8 v[10:13], v[90:93], v[200:203], v[10:13]
	v_mfma_i32_16x16x64_i8 v[62:65], v[86:89], v[180:183], v[62:65]
	v_mfma_i32_16x16x64_i8 v[58:61], v[94:97], v[180:183], v[58:61]
	v_mfma_i32_16x16x64_i8 v[46:49], v[86:89], v[188:191], v[46:49]
	v_mfma_i32_16x16x64_i8 v[42:45], v[94:97], v[188:191], v[42:45]
	v_mfma_i32_16x16x64_i8 v[30:33], v[86:89], v[196:199], v[30:33]
	v_mfma_i32_16x16x64_i8 v[26:29], v[94:97], v[196:199], v[26:29]
	v_mfma_i32_16x16x64_i8 v[14:17], v[86:89], v[204:207], v[14:17]
	v_mfma_i32_16x16x64_i8 v[10:13], v[94:97], v[204:207], v[10:13]
	s_setprio 0
	s_setprio 1
	v_mfma_i32_16x16x64_i8 v[54:57], v[160:163], v[176:179], v[54:57]
	v_mfma_i32_16x16x64_i8 v[50:53], v[168:171], v[176:179], v[50:53]
	v_mfma_i32_16x16x64_i8 v[38:41], v[160:163], v[184:187], v[38:41]
	v_mfma_i32_16x16x64_i8 v[34:37], v[168:171], v[184:187], v[34:37]
	v_mfma_i32_16x16x64_i8 v[22:25], v[160:163], v[192:195], v[22:25]
	v_mfma_i32_16x16x64_i8 v[18:21], v[168:171], v[192:195], v[18:21]
	v_mfma_i32_16x16x64_i8 v[6:9], v[160:163], v[200:203], v[6:9]
	v_mfma_i32_16x16x64_i8 v[2:5], v[168:171], v[200:203], v[2:5]
	v_mfma_i32_16x16x64_i8 v[54:57], v[164:167], v[180:183], v[54:57]
	v_mfma_i32_16x16x64_i8 v[50:53], v[172:175], v[180:183], v[50:53]
	v_mfma_i32_16x16x64_i8 v[38:41], v[164:167], v[188:191], v[38:41]
	v_mfma_i32_16x16x64_i8 v[34:37], v[172:175], v[188:191], v[34:37]
	v_mfma_i32_16x16x64_i8 v[22:25], v[164:167], v[196:199], v[22:25]
	v_mfma_i32_16x16x64_i8 v[18:21], v[172:175], v[196:199], v[18:21]
	v_mfma_i32_16x16x64_i8 v[6:9], v[164:167], v[204:207], v[6:9]
	v_mfma_i32_16x16x64_i8 v[2:5], v[172:175], v[204:207], v[2:5]
	s_setprio 0
	s_barrier
	v_mov_b32_e32 v0, v149
	s_mov_b32 m0, s61
	v_lshl_add_u64 v[146:147], s[42:43], 0, v[0:1]
	v_lshl_add_u64 v[146:147], v[146:147], 0, s[90:91]
	v_mov_b32_e32 v0, v153
	global_load_lds_dwordx4 v[146:147], off
	s_mov_b32 m0, s62
	v_lshl_add_u64 v[146:147], s[42:43], 0, v[0:1]
	v_lshl_add_u64 v[146:147], v[146:147], 0, s[90:91]
	global_load_lds_dwordx4 v[146:147], off
	s_add_i32 s67, s67, 2
	s_add_u32 s40, s40, 0x100
	s_addc_u32 s41, s41, 0
	s_add_u32 s37, s37, 0x100
	s_addc_u32 s66, s66, 0
	s_cmp_gt_u32 s67, 5
	s_cbranch_scc0 .LBB0_1508
	s_lshl_b32 s23, s38, 8
	s_add_i32 s23, s23, s87
	s_mul_i32 s37, s65, 0x5800
	s_mul_hi_i32 s29, s65, 0x5800
	s_add_u32 s37, s59, s37
	s_addc_u32 s29, s60, s29
	s_lshl_b32 s40, s36, 8
	s_ashr_i32 s41, s40, 31
	s_lshl_b64 s[40:41], s[40:41], 2
	s_add_u32 s37, s37, s40
	v_mbcnt_lo_u32_b32 v0, -1, 0
	v_mbcnt_hi_u32_b32 v0, -1, v0
	s_addc_u32 s29, s29, s41
	v_lshrrev_b32_e32 v82, 1, v0
	s_lshl_b32 s38, s72, 2
	v_and_or_b32 v160, v0, 15, s23
	v_and_b32_e32 v162, 24, v82
	s_add_u32 s40, s37, s38
	v_ashrrev_i32_e32 v161, 31, v160
	s_addc_u32 s41, s29, 0
	v_lshlrev_b32_e32 v90, 2, v162
	v_lshl_add_u64 v[146:147], v[160:161], 2, s[20:21]
	global_load_dwordx4 v[86:89], v90, s[40:41] offset:16
	global_load_dwordx4 v[94:97], v90, s[40:41]
	global_load_dwordx4 v[82:85], v90, s[40:41] offset:528
	s_nop 0
	global_load_dwordx4 v[90:93], v90, s[40:41] offset:512
	v_cvt_f32_i32_e32 v173, v143
	global_load_dword v170, v[146:147], off
	global_load_dword v158, v[146:147], off offset:64
	global_load_dword v156, v[146:147], off offset:128
	global_load_dword v154, v[146:147], off offset:192
	global_load_dword v152, v[146:147], off offset:512
	global_load_dword v150, v[146:147], off offset:576
	global_load_dword v148, v[146:147], off offset:640
	global_load_dword v0, v[146:147], off offset:704
	v_cvt_f32_i32_e32 v172, v142
	v_cvt_f32_i32_e32 v143, v145
	v_cvt_f32_i32_e32 v142, v144
	s_lshl_b32 s23, s36, 7
	s_or_b32 s23, s23, s72
	v_or_b32_e32 v146, s23, v162
	v_cvt_f32_i32_e32 v133, v133
	v_cvt_f32_i32_e32 v132, v132
	v_cvt_f32_i32_e32 v131, v131
	v_cvt_f32_i32_e32 v130, v130
	s_mov_b32 s23, 0xc3e00000
	s_movk_i32 s29, 0xb00
	v_cvt_f32_i32_e32 v127, v127
	v_cvt_f32_i32_e32 v126, v126
	v_ashrrev_i32_e32 v147, 31, v146
	v_mov_b64_e32 v[176:177], s[18:19]
	v_mad_i64_i32 v[176:177], s[36:37], v160, s29, v[176:177]
	v_lshl_add_u64 v[176:177], v[176:177], 0, v[146:147]
	s_mov_b32 s41, 0
	s_mov_b32 s40, 0xb000
	v_lshl_add_u64 v[178:179], v[176:177], 0, s[40:41]
	s_mov_b32 s40, 0x16000
	v_lshl_add_u64 v[180:181], v[176:177], 0, s[40:41]
	s_mov_b32 s40, 0x21000
	v_lshl_add_u64 v[182:183], v[176:177], 0, s[40:41]
	s_mov_b32 s40, 0x58000
	v_lshl_add_u64 v[184:185], v[176:177], 0, s[40:41]
	s_mov_b32 s40, 0x63000
	v_lshl_add_u64 v[186:187], v[176:177], 0, s[40:41]
	s_mov_b32 s40, 0x6e000
	v_lshl_add_u64 v[188:189], v[176:177], 0, s[40:41]
	s_mov_b32 s40, 0x79000
	v_lshl_add_u64 v[190:191], v[176:177], 0, s[40:41]
	v_cvt_f32_i32_e32 v129, v129
	v_cvt_f32_i32_e32 v128, v128
	v_cvt_f32_i32_e32 v119, v119
	v_cvt_f32_i32_e32 v118, v118
	v_cvt_f32_i32_e32 v121, v121
	v_cvt_f32_i32_e32 v120, v120
	v_cvt_f32_i32_e32 v123, v123
	v_cvt_f32_i32_e32 v122, v122
	v_cvt_f32_i32_e32 v125, v125
	v_cvt_f32_i32_e32 v124, v124
	v_cvt_f32_i32_e32 v115, v115
	v_cvt_f32_i32_e32 v114, v114
	v_cvt_f32_i32_e32 v117, v117
	v_cvt_f32_i32_e32 v116, v116
	v_cvt_f32_i32_e32 v111, v111
	v_cvt_f32_i32_e32 v110, v110
	v_cvt_f32_i32_e32 v113, v113
	v_cvt_f32_i32_e32 v112, v112
	v_cvt_f32_i32_e32 v103, v103
	v_cvt_f32_i32_e32 v102, v102
	v_cvt_f32_i32_e32 v105, v105
	v_cvt_f32_i32_e32 v104, v104
	v_cvt_f32_i32_e32 v107, v107
	v_cvt_f32_i32_e32 v106, v106
	v_cvt_f32_i32_e32 v109, v109
	v_cvt_f32_i32_e32 v108, v108
	v_cvt_f32_i32_e32 v99, v99
	v_cvt_f32_i32_e32 v98, v98
	v_cvt_f32_i32_e32 v101, v101
	v_cvt_f32_i32_e32 v100, v100
	v_cvt_f32_i32_e32 v79, v79
	v_cvt_f32_i32_e32 v78, v78
	v_readlane_b32 s40, v254, 19
	v_readlane_b32 s41, v254, 20
	s_and_b64 vcc, exec, s[40:41]
	s_cbranch_vccz .LBB0_1511
	s_barrier

.LBB0_1612:
	s_add_u32 s36, s34, 0xfffa8080
	s_addc_u32 s37, s35, -1
	s_add_i32 s61, 0, 0x10000
	s_cmp_eq_u32 s60, 18
	s_cselect_b32 s37, s27, s37
	s_cselect_b32 s36, s26, s36
	v_add_u32_e32 v0, s61, v198
	s_cselect_b32 s39, s29, s59
	s_cselect_b32 s38, s28, s31
	s_add_i32 s64, 0, 0x14000
	ds_read_b128 v[130:133], v0
	ds_read_b128 v[134:137], v0 offset:1024
	ds_read_b128 v[138:141], v0 offset:2048
	ds_read_b128 v[142:145], v0 offset:3072
	v_add_u32_e32 v0, s64, v198
	ds_read_b128 v[146:149], v0
	ds_read_b128 v[150:153], v0 offset:1024
	ds_read_b128 v[154:157], v0 offset:2048
	ds_read_b128 v[158:161], v0 offset:3072
	ds_read_b128 v[162:165], v199
	ds_read_b128 v[166:169], v199 offset:1024
	ds_read_b128 v[170:173], v199 offset:2048
	ds_read_b128 v[174:177], v199 offset:3072
	ds_read_b128 v[178:181], v199 offset:4096
	ds_read_b128 v[182:185], v199 offset:5120
	ds_read_b128 v[186:189], v199 offset:6144
	ds_read_b128 v[190:193], v199 offset:7168
	s_add_i32 m0, s85, 0xc000
	s_nop 0
	global_load_lds_dwordx4 v194, s[34:35]
	s_add_i32 m0, s85, 0xe000
	s_nop 0
	global_load_lds_dwordx4 v196, s[34:35]
	s_waitcnt vmcnt(8)
	s_waitcnt lgkmcnt(0)
	s_barrier
	s_setprio 1
	s_waitcnt lgkmcnt(0)
	v_mfma_scale_f32_16x16x128_f8f6f4 v[126:129], v[130:137], v[162:169], v[126:129], v234, v252 op_sel_hi:[0,0,0]
	v_mfma_scale_f32_16x16x128_f8f6f4 v[122:125], v[138:145], v[162:169], v[122:125], v234, v252 op_sel_hi:[0,0,0]
	v_mfma_scale_f32_16x16x128_f8f6f4 v[118:121], v[130:137], v[170:177], v[118:121], v234, v252 op_sel_hi:[0,0,0]
	v_mfma_scale_f32_16x16x128_f8f6f4 v[114:117], v[138:145], v[170:177], v[114:117], v234, v252 op_sel_hi:[0,0,0]
	v_mfma_scale_f32_16x16x128_f8f6f4 v[110:113], v[130:137], v[178:185], v[110:113], v234, v252 op_sel_hi:[0,0,0]
	v_mfma_scale_f32_16x16x128_f8f6f4 v[106:109], v[138:145], v[178:185], v[106:109], v234, v252 op_sel_hi:[0,0,0]
	v_mfma_scale_f32_16x16x128_f8f6f4 v[102:105], v[130:137], v[186:193], v[102:105], v234, v252 op_sel_hi:[0,0,0]
	v_mfma_scale_f32_16x16x128_f8f6f4 v[98:101], v[138:145], v[186:193], v[98:101], v234, v252 op_sel_hi:[0,0,0]
	s_setprio 0
	s_setprio 1
	v_mfma_scale_f32_16x16x128_f8f6f4 v[200:203], v[146:153], v[162:169], v[62:65], v234, v252 op_sel_hi:[0,0,0]
	v_mfma_scale_f32_16x16x128_f8f6f4 v[162:165], v[154:161], v[162:169], v[58:61], v234, v252 op_sel_hi:[0,0,0]
	v_mfma_scale_f32_16x16x128_f8f6f4 v[166:169], v[146:153], v[170:177], v[54:57], v234, v252 op_sel_hi:[0,0,0]
	v_mfma_scale_f32_16x16x128_f8f6f4 v[170:173], v[154:161], v[170:177], v[50:53], v234, v252 op_sel_hi:[0,0,0]
	v_mfma_scale_f32_16x16x128_f8f6f4 v[174:177], v[146:153], v[178:185], v[46:49], v234, v252 op_sel_hi:[0,0,0]
	v_mfma_scale_f32_16x16x128_f8f6f4 v[178:181], v[154:161], v[178:185], v[42:45], v234, v252 op_sel_hi:[0,0,0]
	v_mfma_scale_f32_16x16x128_f8f6f4 v[182:185], v[146:153], v[186:193], v[38:41], v234, v252 op_sel_hi:[0,0,0]
	v_mfma_scale_f32_16x16x128_f8f6f4 v[186:189], v[154:161], v[186:193], v[34:37], v234, v252 op_sel_hi:[0,0,0]
	s_setprio 0
	s_barrier
	s_add_i32 s61, s61, s33
	s_nop 2
	ds_read_b128 v[34:37], v199 offset:16384
	ds_read_b128 v[38:41], v199 offset:17408
	ds_read_b128 v[42:45], v199 offset:18432
	ds_read_b128 v[46:49], v199 offset:19456
	ds_read_b128 v[50:53], v199 offset:20480
	ds_read_b128 v[54:57], v199 offset:21504
	ds_read_b128 v[58:61], v199 offset:22528
	ds_read_b128 v[62:65], v199 offset:23552
	s_mov_b32 m0, s61
	s_nop 0
	global_load_lds_dwordx4 v195, s[38:39]
	s_add_i32 m0, s61, 0x2000
	s_add_u32 s62, s38, 0x58000
	global_load_lds_dwordx4 v197, s[38:39]
	s_addc_u32 s63, s39, 0
	s_add_i32 s61, s64, s33
	s_mov_b32 m0, s61
	s_nop 0
	global_load_lds_dwordx4 v195, s[62:63]
	s_add_i32 m0, s61, 0x2000
	s_nop 0
	global_load_lds_dwordx4 v197, s[62:63]
	s_waitcnt vmcnt(6)
	s_waitcnt lgkmcnt(0)
	s_barrier
	s_setprio 1
	s_waitcnt lgkmcnt(0)
	v_mfma_scale_f32_16x16x128_f8f6f4 v[94:97], v[130:137], v[34:41], v[94:97], v234, v252 op_sel_hi:[0,0,0]
	v_mfma_scale_f32_16x16x128_f8f6f4 v[90:93], v[138:145], v[34:41], v[90:93], v234, v252 op_sel_hi:[0,0,0]
	v_mfma_scale_f32_16x16x128_f8f6f4 v[86:89], v[130:137], v[42:49], v[86:89], v234, v252 op_sel_hi:[0,0,0]
	v_mfma_scale_f32_16x16x128_f8f6f4 v[82:85], v[138:145], v[42:49], v[82:85], v234, v252 op_sel_hi:[0,0,0]
	v_mfma_scale_f32_16x16x128_f8f6f4 v[78:81], v[130:137], v[50:57], v[78:81], v234, v252 op_sel_hi:[0,0,0]
	v_mfma_scale_f32_16x16x128_f8f6f4 v[74:77], v[138:145], v[50:57], v[74:77], v234, v252 op_sel_hi:[0,0,0]
	v_mfma_scale_f32_16x16x128_f8f6f4 v[190:193], v[130:137], v[58:65], v[70:73], v234, v252 op_sel_hi:[0,0,0]
	v_mfma_scale_f32_16x16x128_f8f6f4 v[204:207], v[138:145], v[58:65], v[66:69], v234, v252 op_sel_hi:[0,0,0]
	s_setprio 0
	s_setprio 1
	v_mfma_scale_f32_16x16x128_f8f6f4 v[208:211], v[146:153], v[34:41], v[30:33], v234, v252 op_sel_hi:[0,0,0]
	v_mfma_scale_f32_16x16x128_f8f6f4 v[212:215], v[154:161], v[34:41], v[26:29], v234, v252 op_sel_hi:[0,0,0]
	v_mfma_scale_f32_16x16x128_f8f6f4 v[216:219], v[146:153], v[42:49], v[22:25], v234, v252 op_sel_hi:[0,0,0]
	v_mfma_scale_f32_16x16x128_f8f6f4 v[228:231], v[154:161], v[42:49], v[18:21], v234, v252 op_sel_hi:[0,0,0]
	v_mfma_scale_f32_16x16x128_f8f6f4 v[244:247], v[146:153], v[50:57], v[14:17], v234, v252 op_sel_hi:[0,0,0]
	v_mfma_scale_f32_16x16x128_f8f6f4 v[248:251], v[154:161], v[50:57], v[10:13], v234, v252 op_sel_hi:[0,0,0]
	v_mfma_scale_f32_16x16x128_f8f6f4 v[224:227], v[146:153], v[58:65], v[6:9], v234, v252 op_sel_hi:[0,0,0]
	v_mfma_scale_f32_16x16x128_f8f6f4 v[220:223], v[154:161], v[58:65], v[2:5], v234, v252 op_sel_hi:[0,0,0]
	s_setprio 0
	s_barrier
	s_add_i32 s61, 0, 0x18000
	v_add_u32_e32 v0, s61, v198
	s_add_i32 s64, 0, 0x1c000
	s_nop 1
	ds_read_b128 v[2:5], v0
	ds_read_b128 v[6:9], v0 offset:1024
	ds_read_b128 v[10:13], v0 offset:2048
	ds_read_b128 v[14:17], v0 offset:3072
	v_add_u32_e32 v0, s64, v198
	ds_read_b128 v[130:133], v0
	ds_read_b128 v[134:137], v0 offset:1024
	ds_read_b128 v[138:141], v0 offset:2048
	ds_read_b128 v[142:145], v0 offset:3072
	s_add_u32 s62, s36, 0x58000
	ds_read_b128 v[18:21], v199 offset:32768
	ds_read_b128 v[22:25], v199 offset:33792
	ds_read_b128 v[26:29], v199 offset:34816
	ds_read_b128 v[30:33], v199 offset:35840
	ds_read_b128 v[34:37], v199 offset:36864
	ds_read_b128 v[38:41], v199 offset:37888
	ds_read_b128 v[66:69], v199 offset:38912
	ds_read_b128 v[70:73], v199 offset:39936
	s_addc_u32 s63, s37, 0
	s_mov_b32 m0, s85
	s_nop 0
	global_load_lds_dwordx4 v194, s[36:37]
	s_mov_b32 m0, s3
	s_nop 0
	global_load_lds_dwordx4 v196, s[36:37]
	s_mov_b32 m0, s45
	s_nop 0
	global_load_lds_dwordx4 v194, s[62:63]
	s_mov_b32 m0, s47
	s_nop 0
	global_load_lds_dwordx4 v196, s[62:63]
	s_waitcnt vmcnt(8)
	s_waitcnt lgkmcnt(0)
	s_barrier
	s_setprio 1
	s_waitcnt lgkmcnt(0)
	v_mfma_scale_f32_16x16x128_f8f6f4 v[126:129], v[2:9], v[18:25], v[126:129], v234, v252 op_sel_hi:[0,0,0]
	v_mfma_scale_f32_16x16x128_f8f6f4 v[122:125], v[10:17], v[18:25], v[122:125], v234, v252 op_sel_hi:[0,0,0]
	v_mfma_scale_f32_16x16x128_f8f6f4 v[118:121], v[2:9], v[26:33], v[118:121], v234, v252 op_sel_hi:[0,0,0]
	v_mfma_scale_f32_16x16x128_f8f6f4 v[114:117], v[10:17], v[26:33], v[114:117], v234, v252 op_sel_hi:[0,0,0]
	v_mfma_scale_f32_16x16x128_f8f6f4 v[110:113], v[2:9], v[34:41], v[110:113], v234, v252 op_sel_hi:[0,0,0]
	v_mfma_scale_f32_16x16x128_f8f6f4 v[106:109], v[10:17], v[34:41], v[106:109], v234, v252 op_sel_hi:[0,0,0]
	v_mfma_scale_f32_16x16x128_f8f6f4 v[102:105], v[2:9], v[66:73], v[102:105], v234, v252 op_sel_hi:[0,0,0]
	v_mfma_scale_f32_16x16x128_f8f6f4 v[98:101], v[10:17], v[66:73], v[98:101], v234, v252 op_sel_hi:[0,0,0]
	s_setprio 0
	s_setprio 1
	v_mfma_scale_f32_16x16x128_f8f6f4 v[62:65], v[130:137], v[18:25], v[200:203], v234, v252 op_sel_hi:[0,0,0]
	v_mfma_scale_f32_16x16x128_f8f6f4 v[58:61], v[138:145], v[18:25], v[162:165], v234, v252 op_sel_hi:[0,0,0]
	v_mfma_scale_f32_16x16x128_f8f6f4 v[54:57], v[130:137], v[26:33], v[166:169], v234, v252 op_sel_hi:[0,0,0]
	v_mfma_scale_f32_16x16x128_f8f6f4 v[50:53], v[138:145], v[26:33], v[170:173], v234, v252 op_sel_hi:[0,0,0]
	v_mfma_scale_f32_16x16x128_f8f6f4 v[46:49], v[130:137], v[34:41], v[174:177], v234, v252 op_sel_hi:[0,0,0]
	v_mfma_scale_f32_16x16x128_f8f6f4 v[42:45], v[138:145], v[34:41], v[178:181], v234, v252 op_sel_hi:[0,0,0]
	v_mfma_scale_f32_16x16x128_f8f6f4 v[38:41], v[130:137], v[66:73], v[182:185], v234, v252 op_sel_hi:[0,0,0]
	v_mfma_scale_f32_16x16x128_f8f6f4 v[34:37], v[138:145], v[66:73], v[186:189], v234, v252 op_sel_hi:[0,0,0]
	s_setprio 0
	s_barrier
	v_mov_b32_e32 v0, v195
	ds_read_b128 v[18:21], v199 offset:49152
	ds_read_b128 v[22:25], v199 offset:50176
	ds_read_b128 v[146:149], v199 offset:51200
	ds_read_b128 v[150:153], v199 offset:52224
	ds_read_b128 v[154:157], v199 offset:53248
	ds_read_b128 v[158:161], v199 offset:54272
	ds_read_b128 v[162:165], v199 offset:55296
	ds_read_b128 v[166:169], v199 offset:56320
	s_add_i32 s61, s61, s33
	v_lshl_add_u64 v[26:27], s[38:39], 0, v[0:1]
	v_lshl_add_u64 v[26:27], v[26:27], 0, s[90:91]
	s_mov_b32 m0, s61
	v_mov_b32_e32 v0, v197
	global_load_lds_dwordx4 v[26:27], off
	s_add_i32 m0, s61, 0x2000
	s_nop 0
	v_lshl_add_u64 v[26:27], s[38:39], 0, v[0:1]
	s_add_u32 s38, s38, 0x58080
	v_lshl_add_u64 v[26:27], v[26:27], 0, s[90:91]
	s_addc_u32 s39, s39, 0
	s_add_i32 s61, s64, s33
	global_load_lds_dwordx4 v[26:27], off
	s_mov_b32 m0, s61
	s_nop 0
	global_load_lds_dwordx4 v195, s[38:39]
	s_add_i32 m0, s61, 0x2000
	s_nop 0
	global_load_lds_dwordx4 v197, s[38:39]
	s_waitcnt vmcnt(6)
	s_waitcnt lgkmcnt(0)
	s_barrier
	s_setprio 1
	s_waitcnt lgkmcnt(0)
	v_mfma_scale_f32_16x16x128_f8f6f4 v[94:97], v[2:9], v[18:25], v[94:97], v234, v252 op_sel_hi:[0,0,0]
	v_mfma_scale_f32_16x16x128_f8f6f4 v[90:93], v[10:17], v[18:25], v[90:93], v234, v252 op_sel_hi:[0,0,0]
	v_mfma_scale_f32_16x16x128_f8f6f4 v[86:89], v[2:9], v[146:153], v[86:89], v234, v252 op_sel_hi:[0,0,0]
	v_mfma_scale_f32_16x16x128_f8f6f4 v[82:85], v[10:17], v[146:153], v[82:85], v234, v252 op_sel_hi:[0,0,0]
	v_mfma_scale_f32_16x16x128_f8f6f4 v[78:81], v[2:9], v[154:161], v[78:81], v234, v252 op_sel_hi:[0,0,0]
	v_mfma_scale_f32_16x16x128_f8f6f4 v[74:77], v[10:17], v[154:161], v[74:77], v234, v252 op_sel_hi:[0,0,0]
	v_mfma_scale_f32_16x16x128_f8f6f4 v[70:73], v[2:9], v[162:169], v[190:193], v234, v252 op_sel_hi:[0,0,0]
	v_mfma_scale_f32_16x16x128_f8f6f4 v[66:69], v[10:17], v[162:169], v[204:207], v234, v252 op_sel_hi:[0,0,0]
	s_setprio 0
	s_setprio 1
	v_mfma_scale_f32_16x16x128_f8f6f4 v[30:33], v[130:137], v[18:25], v[208:211], v234, v252 op_sel_hi:[0,0,0]
	v_mfma_scale_f32_16x16x128_f8f6f4 v[26:29], v[138:145], v[18:25], v[212:215], v234, v252 op_sel_hi:[0,0,0]
	v_mfma_scale_f32_16x16x128_f8f6f4 v[22:25], v[130:137], v[146:153], v[216:219], v234, v252 op_sel_hi:[0,0,0]
	v_mfma_scale_f32_16x16x128_f8f6f4 v[18:21], v[138:145], v[146:153], v[228:231], v234, v252 op_sel_hi:[0,0,0]
	v_mfma_scale_f32_16x16x128_f8f6f4 v[14:17], v[130:137], v[154:161], v[244:247], v234, v252 op_sel_hi:[0,0,0]
	v_mfma_scale_f32_16x16x128_f8f6f4 v[10:13], v[138:145], v[154:161], v[248:251], v234, v252 op_sel_hi:[0,0,0]
	v_mfma_scale_f32_16x16x128_f8f6f4 v[6:9], v[130:137], v[162:169], v[224:227], v234, v252 op_sel_hi:[0,0,0]
	v_mfma_scale_f32_16x16x128_f8f6f4 v[2:5], v[138:145], v[162:169], v[220:223], v234, v252 op_sel_hi:[0,0,0]
	s_setprio 0
	s_barrier
	v_mov_b32_e32 v0, v194
	s_mov_b32 m0, s50
	v_lshl_add_u64 v[190:191], s[36:37], 0, v[0:1]
	v_lshl_add_u64 v[190:191], v[190:191], 0, s[90:91]
	v_mov_b32_e32 v0, v196
	global_load_lds_dwordx4 v[190:191], off
	s_mov_b32 m0, s51
	v_lshl_add_u64 v[190:191], s[36:37], 0, v[0:1]
	v_lshl_add_u64 v[190:191], v[190:191], 0, s[90:91]
	global_load_lds_dwordx4 v[190:191], off
	s_add_i32 s60, s60, 2
	s_add_u32 s34, s34, 0x100
	s_addc_u32 s35, s35, 0
	s_add_u32 s31, s31, 0x100
	s_addc_u32 s59, s59, 0
	s_cmp_gt_u32 s60, 19
	s_cbranch_scc0 .LBB0_1612
	v_readlane_b32 s34, v254, 19
	v_readlane_b32 s35, v254, 20
	s_and_b64 vcc, exec, s[34:35]
	s_cbranch_vccz .LBB0_1615
	s_barrier

.LBB0_1670:
	s_add_u32 s36, s34, 0xfffa8080
	s_addc_u32 s37, s35, -1
	s_add_i32 s60, 0, 0x10000
	s_cmp_eq_u32 s59, 18
	s_cselect_b32 s37, s27, s37
	s_cselect_b32 s36, s26, s36
	v_add_u32_e32 v0, s60, v143
	s_cselect_b32 s39, s29, s58
	s_cselect_b32 s38, s28, s31
	s_add_i32 s62, 0, 0x14000
	ds_read_b128 v[146:149], v0
	ds_read_b128 v[150:153], v0 offset:1024
	ds_read_b128 v[154:157], v0 offset:2048
	ds_read_b128 v[158:161], v0 offset:3072
	v_add_u32_e32 v0, s62, v143
	ds_read_b128 v[162:165], v0
	ds_read_b128 v[166:169], v0 offset:1024
	ds_read_b128 v[170:173], v0 offset:2048
	ds_read_b128 v[174:177], v0 offset:3072
	ds_read_b128 v[178:181], v145
	ds_read_b128 v[182:185], v145 offset:1024
	ds_read_b128 v[186:189], v145 offset:2048
	ds_read_b128 v[190:193], v145 offset:3072
	ds_read_b128 v[194:197], v145 offset:4096
	ds_read_b128 v[198:201], v145 offset:5120
	ds_read_b128 v[202:205], v145 offset:6144
	ds_read_b128 v[206:209], v145 offset:7168
	s_add_i32 m0, s85, 0xc000
	s_nop 0
	global_load_lds_dwordx4 v253, s[34:35]
	s_add_i32 m0, s85, 0xe000
	s_nop 0
	global_load_lds_dwordx4 v242, s[34:35]
	s_waitcnt vmcnt(8)
	s_waitcnt lgkmcnt(0)
	s_barrier
	s_setprio 1
	s_waitcnt lgkmcnt(0)
	v_mfma_scale_f32_16x16x128_f8f6f4 v[126:129], v[146:153], v[178:185], v[126:129], v234, v252 op_sel_hi:[0,0,0]
	v_mfma_scale_f32_16x16x128_f8f6f4 v[122:125], v[154:161], v[178:185], v[122:125], v234, v252 op_sel_hi:[0,0,0]
	v_mfma_scale_f32_16x16x128_f8f6f4 v[110:113], v[146:153], v[186:193], v[110:113], v234, v252 op_sel_hi:[0,0,0]
	v_mfma_scale_f32_16x16x128_f8f6f4 v[106:109], v[154:161], v[186:193], v[106:109], v234, v252 op_sel_hi:[0,0,0]
	v_mfma_scale_f32_16x16x128_f8f6f4 v[210:213], v[146:153], v[194:201], v[94:97], v234, v252 op_sel_hi:[0,0,0]
	v_mfma_scale_f32_16x16x128_f8f6f4 v[214:217], v[154:161], v[194:201], v[90:93], v234, v252 op_sel_hi:[0,0,0]
	v_mfma_scale_f32_16x16x128_f8f6f4 v[218:221], v[146:153], v[202:209], v[78:81], v234, v252 op_sel_hi:[0,0,0]
	v_mfma_scale_f32_16x16x128_f8f6f4 v[222:225], v[154:161], v[202:209], v[74:77], v234, v252 op_sel_hi:[0,0,0]
	s_setprio 0
	s_setprio 1
	v_mfma_scale_f32_16x16x128_f8f6f4 v[118:121], v[162:169], v[178:185], v[118:121], v234, v252 op_sel_hi:[0,0,0]
	v_mfma_scale_f32_16x16x128_f8f6f4 v[114:117], v[170:177], v[178:185], v[114:117], v234, v252 op_sel_hi:[0,0,0]
	v_mfma_scale_f32_16x16x128_f8f6f4 v[102:105], v[162:169], v[186:193], v[102:105], v234, v252 op_sel_hi:[0,0,0]
	v_mfma_scale_f32_16x16x128_f8f6f4 v[98:101], v[170:177], v[186:193], v[98:101], v234, v252 op_sel_hi:[0,0,0]
	v_mfma_scale_f32_16x16x128_f8f6f4 v[178:181], v[162:169], v[194:201], v[86:89], v234, v252 op_sel_hi:[0,0,0]
	v_mfma_scale_f32_16x16x128_f8f6f4 v[182:185], v[170:177], v[194:201], v[82:85], v234, v252 op_sel_hi:[0,0,0]
	v_mfma_scale_f32_16x16x128_f8f6f4 v[186:189], v[162:169], v[202:209], v[70:73], v234, v252 op_sel_hi:[0,0,0]
	v_mfma_scale_f32_16x16x128_f8f6f4 v[190:193], v[170:177], v[202:209], v[66:69], v234, v252 op_sel_hi:[0,0,0]
	s_setprio 0
	s_barrier
	s_add_i32 s60, s60, s33
	s_nop 2
	ds_read_b128 v[66:69], v145 offset:16384
	ds_read_b128 v[70:73], v145 offset:17408
	ds_read_b128 v[74:77], v145 offset:18432
	ds_read_b128 v[78:81], v145 offset:19456
	ds_read_b128 v[82:85], v145 offset:20480
	ds_read_b128 v[86:89], v145 offset:21504
	ds_read_b128 v[90:93], v145 offset:22528
	ds_read_b128 v[94:97], v145 offset:23552
	s_mov_b32 m0, s60
	s_nop 0
	global_load_lds_dwordx4 v243, s[38:39]
	s_add_i32 m0, s60, 0x2000
	s_add_u32 s60, s38, 0x58000
	global_load_lds_dwordx4 v142, s[38:39]
	s_addc_u32 s61, s39, 0
	s_add_i32 s62, s62, s33
	s_mov_b32 m0, s62
	s_nop 0
	global_load_lds_dwordx4 v243, s[60:61]
	s_add_i32 m0, s62, 0x2000
	s_nop 0
	global_load_lds_dwordx4 v142, s[60:61]
	s_waitcnt vmcnt(6)
	s_waitcnt lgkmcnt(0)
	s_barrier
	s_setprio 1
	s_waitcnt lgkmcnt(0)
	v_mfma_scale_f32_16x16x128_f8f6f4 v[62:65], v[146:153], v[66:73], v[62:65], v234, v252 op_sel_hi:[0,0,0]
	v_mfma_scale_f32_16x16x128_f8f6f4 v[58:61], v[154:161], v[66:73], v[58:61], v234, v252 op_sel_hi:[0,0,0]
	v_mfma_scale_f32_16x16x128_f8f6f4 v[54:57], v[146:153], v[74:81], v[54:57], v234, v252 op_sel_hi:[0,0,0]
	v_mfma_scale_f32_16x16x128_f8f6f4 v[194:197], v[154:161], v[74:81], v[46:49], v234, v252 op_sel_hi:[0,0,0]
	v_mfma_scale_f32_16x16x128_f8f6f4 v[198:201], v[146:153], v[82:89], v[38:41], v234, v252 op_sel_hi:[0,0,0]
	v_mfma_scale_f32_16x16x128_f8f6f4 v[202:205], v[154:161], v[82:89], v[30:33], v234, v252 op_sel_hi:[0,0,0]
	v_mfma_scale_f32_16x16x128_f8f6f4 v[206:209], v[146:153], v[90:97], v[22:25], v234, v252 op_sel_hi:[0,0,0]
	v_mfma_scale_f32_16x16x128_f8f6f4 v[226:229], v[154:161], v[90:97], v[14:17], v234, v252 op_sel_hi:[0,0,0]
	s_setprio 0
	s_setprio 1
	v_mfma_scale_f32_16x16x128_f8f6f4 v[50:53], v[162:169], v[66:73], v[50:53], v234, v252 op_sel_hi:[0,0,0]
	v_mfma_scale_f32_16x16x128_f8f6f4 v[244:247], v[170:177], v[66:73], v[42:45], v234, v252 op_sel_hi:[0,0,0]
	v_mfma_scale_f32_16x16x128_f8f6f4 v[248:251], v[162:169], v[74:81], v[34:37], v234, v252 op_sel_hi:[0,0,0]
	v_mfma_scale_f32_16x16x128_f8f6f4 v[236:239], v[170:177], v[74:81], v[26:29], v234, v252 op_sel_hi:[0,0,0]
	v_mfma_scale_f32_16x16x128_f8f6f4 v[230:233], v[162:169], v[82:89], v[18:21], v234, v252 op_sel_hi:[0,0,0]
	v_mfma_scale_f32_16x16x128_f8f6f4 v[130:133], v[170:177], v[82:89], v[10:13], v234, v252 op_sel_hi:[0,0,0]
	v_mfma_scale_f32_16x16x128_f8f6f4 v[134:137], v[162:169], v[90:97], v[6:9], v234, v252 op_sel_hi:[0,0,0]
	v_mfma_scale_f32_16x16x128_f8f6f4 v[138:141], v[170:177], v[90:97], v[2:5], v234, v252 op_sel_hi:[0,0,0]
	s_setprio 0
	s_barrier
	s_add_i32 s62, 0, 0x18000
	v_add_u32_e32 v0, s62, v143
	s_add_i32 s63, 0, 0x1c000
	s_nop 1
	ds_read_b128 v[2:5], v0
	ds_read_b128 v[6:9], v0 offset:1024
	ds_read_b128 v[10:13], v0 offset:2048
	ds_read_b128 v[14:17], v0 offset:3072
	v_add_u32_e32 v0, s63, v143
	ds_read_b128 v[146:149], v0
	ds_read_b128 v[150:153], v0 offset:1024
	ds_read_b128 v[154:157], v0 offset:2048
	ds_read_b128 v[158:161], v0 offset:3072
	s_add_u32 s60, s36, 0x58000
	ds_read_b128 v[18:21], v145 offset:32768
	ds_read_b128 v[22:25], v145 offset:33792
	ds_read_b128 v[26:29], v145 offset:34816
	ds_read_b128 v[30:33], v145 offset:35840
	ds_read_b128 v[34:37], v145 offset:36864
	ds_read_b128 v[38:41], v145 offset:37888
	ds_read_b128 v[42:45], v145 offset:38912
	ds_read_b128 v[46:49], v145 offset:39936
	s_addc_u32 s61, s37, 0
	s_mov_b32 m0, s85
	s_nop 0
	global_load_lds_dwordx4 v253, s[36:37]
	s_mov_b32 m0, s50
	s_nop 0
	global_load_lds_dwordx4 v242, s[36:37]
	s_mov_b32 m0, s51
	s_nop 0
	global_load_lds_dwordx4 v253, s[60:61]
	s_mov_b32 m0, s52
	s_nop 0
	global_load_lds_dwordx4 v242, s[60:61]
	s_waitcnt vmcnt(8)
	s_waitcnt lgkmcnt(0)
	s_barrier
	s_setprio 1
	s_waitcnt lgkmcnt(0)
	v_mfma_scale_f32_16x16x128_f8f6f4 v[126:129], v[2:9], v[18:25], v[126:129], v234, v252 op_sel_hi:[0,0,0]
	v_mfma_scale_f32_16x16x128_f8f6f4 v[122:125], v[10:17], v[18:25], v[122:125], v234, v252 op_sel_hi:[0,0,0]
	v_mfma_scale_f32_16x16x128_f8f6f4 v[110:113], v[2:9], v[26:33], v[110:113], v234, v252 op_sel_hi:[0,0,0]
	v_mfma_scale_f32_16x16x128_f8f6f4 v[106:109], v[10:17], v[26:33], v[106:109], v234, v252 op_sel_hi:[0,0,0]
	v_mfma_scale_f32_16x16x128_f8f6f4 v[94:97], v[2:9], v[34:41], v[210:213], v234, v252 op_sel_hi:[0,0,0]
	v_mfma_scale_f32_16x16x128_f8f6f4 v[90:93], v[10:17], v[34:41], v[214:217], v234, v252 op_sel_hi:[0,0,0]
	v_mfma_scale_f32_16x16x128_f8f6f4 v[78:81], v[2:9], v[42:49], v[218:221], v234, v252 op_sel_hi:[0,0,0]
	v_mfma_scale_f32_16x16x128_f8f6f4 v[74:77], v[10:17], v[42:49], v[222:225], v234, v252 op_sel_hi:[0,0,0]
	s_setprio 0
	s_setprio 1
	v_mfma_scale_f32_16x16x128_f8f6f4 v[118:121], v[146:153], v[18:25], v[118:121], v234, v252 op_sel_hi:[0,0,0]
	v_mfma_scale_f32_16x16x128_f8f6f4 v[114:117], v[154:161], v[18:25], v[114:117], v234, v252 op_sel_hi:[0,0,0]
	v_mfma_scale_f32_16x16x128_f8f6f4 v[102:105], v[146:153], v[26:33], v[102:105], v234, v252 op_sel_hi:[0,0,0]
	v_mfma_scale_f32_16x16x128_f8f6f4 v[98:101], v[154:161], v[26:33], v[98:101], v234, v252 op_sel_hi:[0,0,0]
	v_mfma_scale_f32_16x16x128_f8f6f4 v[86:89], v[146:153], v[34:41], v[178:181], v234, v252 op_sel_hi:[0,0,0]
	v_mfma_scale_f32_16x16x128_f8f6f4 v[82:85], v[154:161], v[34:41], v[182:185], v234, v252 op_sel_hi:[0,0,0]
	v_mfma_scale_f32_16x16x128_f8f6f4 v[70:73], v[146:153], v[42:49], v[186:189], v234, v252 op_sel_hi:[0,0,0]
	v_mfma_scale_f32_16x16x128_f8f6f4 v[66:69], v[154:161], v[42:49], v[190:193], v234, v252 op_sel_hi:[0,0,0]
	s_setprio 0
	s_barrier
	v_mov_b32_e32 v0, v243
	ds_read_b128 v[162:165], v145 offset:49152
	ds_read_b128 v[166:169], v145 offset:50176
	ds_read_b128 v[170:173], v145 offset:51200
	ds_read_b128 v[174:177], v145 offset:52224
	ds_read_b128 v[178:181], v145 offset:53248
	ds_read_b128 v[182:185], v145 offset:54272
	ds_read_b128 v[186:189], v145 offset:55296
	ds_read_b128 v[190:193], v145 offset:56320
	s_add_i32 s60, s62, s33
	v_lshl_add_u64 v[18:19], s[38:39], 0, v[0:1]
	v_lshl_add_u64 v[18:19], v[18:19], 0, s[90:91]
	s_mov_b32 m0, s60
	v_mov_b32_e32 v0, v142
	global_load_lds_dwordx4 v[18:19], off
	s_add_i32 m0, s60, 0x2000
	s_nop 0
	v_lshl_add_u64 v[18:19], s[38:39], 0, v[0:1]
	s_add_u32 s38, s38, 0x58080
	v_lshl_add_u64 v[18:19], v[18:19], 0, s[90:91]
	s_addc_u32 s39, s39, 0
	s_add_i32 s60, s63, s33
	global_load_lds_dwordx4 v[18:19], off
	s_mov_b32 m0, s60
	s_nop 0
	global_load_lds_dwordx4 v243, s[38:39]
	s_add_i32 m0, s60, 0x2000
	s_nop 0
	global_load_lds_dwordx4 v142, s[38:39]
	s_waitcnt vmcnt(6)
	s_waitcnt lgkmcnt(0)
	s_barrier
	s_setprio 1
	s_waitcnt lgkmcnt(0)
	v_mfma_scale_f32_16x16x128_f8f6f4 v[62:65], v[2:9], v[162:169], v[62:65], v234, v252 op_sel_hi:[0,0,0]
	v_mfma_scale_f32_16x16x128_f8f6f4 v[58:61], v[10:17], v[162:169], v[58:61], v234, v252 op_sel_hi:[0,0,0]
	v_mfma_scale_f32_16x16x128_f8f6f4 v[54:57], v[2:9], v[170:177], v[54:57], v234, v252 op_sel_hi:[0,0,0]
	v_mfma_scale_f32_16x16x128_f8f6f4 v[46:49], v[10:17], v[170:177], v[194:197], v234, v252 op_sel_hi:[0,0,0]
	v_mfma_scale_f32_16x16x128_f8f6f4 v[38:41], v[2:9], v[178:185], v[198:201], v234, v252 op_sel_hi:[0,0,0]
	v_mfma_scale_f32_16x16x128_f8f6f4 v[30:33], v[10:17], v[178:185], v[202:205], v234, v252 op_sel_hi:[0,0,0]
	v_mfma_scale_f32_16x16x128_f8f6f4 v[22:25], v[2:9], v[186:193], v[206:209], v234, v252 op_sel_hi:[0,0,0]
	v_mfma_scale_f32_16x16x128_f8f6f4 v[14:17], v[10:17], v[186:193], v[226:229], v234, v252 op_sel_hi:[0,0,0]
	s_setprio 0
	s_setprio 1
	v_mfma_scale_f32_16x16x128_f8f6f4 v[50:53], v[146:153], v[162:169], v[50:53], v234, v252 op_sel_hi:[0,0,0]
	v_mfma_scale_f32_16x16x128_f8f6f4 v[42:45], v[154:161], v[162:169], v[244:247], v234, v252 op_sel_hi:[0,0,0]
	v_mfma_scale_f32_16x16x128_f8f6f4 v[34:37], v[146:153], v[170:177], v[248:251], v234, v252 op_sel_hi:[0,0,0]
	v_mfma_scale_f32_16x16x128_f8f6f4 v[26:29], v[154:161], v[170:177], v[236:239], v234, v252 op_sel_hi:[0,0,0]
	v_mfma_scale_f32_16x16x128_f8f6f4 v[18:21], v[146:153], v[178:185], v[230:233], v234, v252 op_sel_hi:[0,0,0]
	v_mfma_scale_f32_16x16x128_f8f6f4 v[10:13], v[154:161], v[178:185], v[130:133], v234, v252 op_sel_hi:[0,0,0]
	v_mfma_scale_f32_16x16x128_f8f6f4 v[6:9], v[146:153], v[186:193], v[134:137], v234, v252 op_sel_hi:[0,0,0]
	v_mfma_scale_f32_16x16x128_f8f6f4 v[2:5], v[154:161], v[186:193], v[138:141], v234, v252 op_sel_hi:[0,0,0]
	s_setprio 0
	s_barrier
	v_mov_b32_e32 v0, v253
	s_mov_b32 m0, s53
	v_lshl_add_u64 v[198:199], s[36:37], 0, v[0:1]
	v_lshl_add_u64 v[198:199], v[198:199], 0, s[90:91]
	v_mov_b32_e32 v0, v242
	global_load_lds_dwordx4 v[198:199], off
	s_mov_b32 m0, s54
	v_lshl_add_u64 v[198:199], s[36:37], 0, v[0:1]
	v_lshl_add_u64 v[198:199], v[198:199], 0, s[90:91]
	global_load_lds_dwordx4 v[198:199], off
	s_add_i32 s59, s59, 2
	s_add_u32 s34, s34, 0x100
	s_addc_u32 s35, s35, 0
	s_add_u32 s31, s31, 0x100
	s_addc_u32 s58, s58, 0
	s_cmp_gt_u32 s59, 19
	s_cbranch_scc0 .LBB0_1670
	v_readlane_b32 s34, v254, 19
	v_readlane_b32 s35, v254, 20
	s_and_b64 vcc, exec, s[34:35]
	s_cbranch_vccz .LBB0_1673
	s_barrier
